# t2 + GEMM sub-phase hand-off: s_setprio 1 issued before the mid barrier, duplicate lgkmcnt(0) wait after it removed (36 sites)
# speedup vs baseline: 1.0075x; 1.0075x over previous
.LBB0_234:
	s_add_u32 s38, s0, 0xfffc0080
	s_addc_u32 s39, s1, -1
	s_add_i32 s63, 0, 0x10000
	s_cmp_eq_u32 s62, 12
	s_cselect_b32 s41, s25, s39
	s_cselect_b32 s40, s58, s38
	s_cselect_b32 s39, s27, s61
	s_cselect_b32 s38, s59, s60
	s_add_i32 s66, 0, 0x14000
	v_add_u32_e32 v134, s63, v165
	v_add_u32_e32 v160, s66, v165
	ds_read_b128 v[114:117], v134
	ds_read_b128 v[118:121], v134 offset:1024
	ds_read_b128 v[130:133], v134 offset:2048
	ds_read_b128 v[134:137], v134 offset:3072
	ds_read_b128 v[170:173], v160
	ds_read_b128 v[174:177], v160 offset:1024
	ds_read_b128 v[200:203], v160 offset:2048
	ds_read_b128 v[204:207], v160 offset:3072
	v_lshl_add_u64 v[160:161], s[0:1], 0, v[158:159]
	s_add_i32 m0, s37, 0xc000
	ds_read_b128 v[208:211], v168
	ds_read_b128 v[212:215], v168 offset:1024
	ds_read_b128 v[216:219], v168 offset:2048
	ds_read_b128 v[220:223], v168 offset:3072
	ds_read_b128 v[224:227], v168 offset:4096
	ds_read_b128 v[228:231], v168 offset:5120
	ds_read_b128 v[232:235], v168 offset:6144
	ds_read_b128 v[236:239], v168 offset:7168
	global_load_lds_dwordx4 v[160:161], off
	v_lshl_add_u64 v[160:161], s[0:1], 0, v[156:157]
	s_add_i32 m0, s37, 0xe000
	s_nop 0
	global_load_lds_dwordx4 v[160:161], off
	s_waitcnt vmcnt(8)
	s_waitcnt lgkmcnt(0)
	s_setprio 1
	s_barrier
	v_mfma_f32_16x16x32_bf16 v[142:145], v[114:117], v[208:211], v[142:145]
	v_mfma_f32_16x16x32_bf16 v[138:141], v[130:133], v[208:211], v[138:141]
	v_mfma_f32_16x16x32_bf16 v[110:113], v[114:117], v[216:219], v[110:113]
	v_mfma_f32_16x16x32_bf16 v[106:109], v[130:133], v[216:219], v[106:109]
	v_mfma_f32_16x16x32_bf16 v[94:97], v[114:117], v[224:227], v[94:97]
	v_mfma_f32_16x16x32_bf16 v[90:93], v[130:133], v[224:227], v[90:93]
	v_mfma_f32_16x16x32_bf16 v[78:81], v[114:117], v[232:235], v[78:81]
	v_mfma_f32_16x16x32_bf16 v[74:77], v[130:133], v[232:235], v[74:77]
	v_mfma_f32_16x16x32_bf16 v[142:145], v[118:121], v[212:215], v[142:145]
	v_mfma_f32_16x16x32_bf16 v[138:141], v[134:137], v[212:215], v[138:141]
	v_mfma_f32_16x16x32_bf16 v[110:113], v[118:121], v[220:223], v[110:113]
	v_mfma_f32_16x16x32_bf16 v[106:109], v[134:137], v[220:223], v[106:109]
	v_mfma_f32_16x16x32_bf16 v[94:97], v[118:121], v[228:231], v[94:97]
	v_mfma_f32_16x16x32_bf16 v[90:93], v[134:137], v[228:231], v[90:93]
	v_mfma_f32_16x16x32_bf16 v[78:81], v[118:121], v[236:239], v[78:81]
	v_mfma_f32_16x16x32_bf16 v[74:77], v[134:137], v[236:239], v[74:77]
	s_setprio 0
	s_setprio 1
	v_mfma_f32_16x16x32_bf16 v[126:129], v[170:173], v[208:211], v[126:129]
	v_mfma_f32_16x16x32_bf16 v[122:125], v[200:203], v[208:211], v[122:125]
	v_mfma_f32_16x16x32_bf16 v[102:105], v[170:173], v[216:219], v[102:105]
	v_mfma_f32_16x16x32_bf16 v[98:101], v[200:203], v[216:219], v[98:101]
	v_mfma_f32_16x16x32_bf16 v[86:89], v[170:173], v[224:227], v[86:89]
	v_mfma_f32_16x16x32_bf16 v[82:85], v[200:203], v[224:227], v[82:85]
	v_mfma_f32_16x16x32_bf16 v[70:73], v[170:173], v[232:235], v[70:73]
	v_mfma_f32_16x16x32_bf16 v[66:69], v[200:203], v[232:235], v[66:69]
	v_mfma_f32_16x16x32_bf16 v[126:129], v[174:177], v[212:215], v[126:129]
	v_mfma_f32_16x16x32_bf16 v[122:125], v[204:207], v[212:215], v[122:125]
	v_mfma_f32_16x16x32_bf16 v[102:105], v[174:177], v[220:223], v[102:105]
	v_mfma_f32_16x16x32_bf16 v[98:101], v[204:207], v[220:223], v[98:101]
	v_mfma_f32_16x16x32_bf16 v[86:89], v[174:177], v[228:231], v[86:89]
	v_mfma_f32_16x16x32_bf16 v[82:85], v[204:207], v[228:231], v[82:85]
	v_mfma_f32_16x16x32_bf16 v[70:73], v[174:177], v[236:239], v[70:73]
	v_mfma_f32_16x16x32_bf16 v[66:69], v[204:207], v[236:239], v[66:69]
	s_setprio 0
	s_barrier
	s_add_i32 s63, s63, s42
	v_lshl_add_u64 v[160:161], s[38:39], 0, v[146:147]
	s_mov_b32 m0, s63
	ds_read_b128 v[208:211], v168 offset:16384
	ds_read_b128 v[212:215], v168 offset:17408
	ds_read_b128 v[216:219], v168 offset:18432
	ds_read_b128 v[220:223], v168 offset:19456
	ds_read_b128 v[224:227], v168 offset:20480
	ds_read_b128 v[228:231], v168 offset:21504
	ds_read_b128 v[232:235], v168 offset:22528
	ds_read_b128 v[236:239], v168 offset:23552
	global_load_lds_dwordx4 v[160:161], off
	s_add_i32 m0, s63, 0x2000
	s_add_u32 s64, s38, 0x40000
	v_lshl_add_u64 v[178:179], s[38:39], 0, v[148:149]
	s_addc_u32 s65, s39, 0
	s_add_i32 s63, s66, s42
	global_load_lds_dwordx4 v[178:179], off
	v_lshl_add_u64 v[240:241], s[64:65], 0, v[146:147]
	s_mov_b32 m0, s63
	v_lshl_add_u64 v[242:243], s[40:41], 0, v[148:149]
	global_load_lds_dwordx4 v[240:241], off
	v_lshl_add_u64 v[240:241], s[64:65], 0, v[148:149]
	s_add_i32 m0, s63, 0x2000
	s_nop 0
	global_load_lds_dwordx4 v[240:241], off
	v_lshl_add_u64 v[240:241], s[40:41], 0, v[146:147]
	s_mov_b32 m0, s37
	s_nop 0
	global_load_lds_dwordx4 v[240:241], off
	s_mov_b32 m0, s47
	s_nop 0
	global_load_lds_dwordx4 v[242:243], off
	s_waitcnt vmcnt(8)
	s_waitcnt lgkmcnt(0)
	s_setprio 1
	s_barrier
	v_mfma_f32_16x16x32_bf16 v[62:65], v[114:117], v[208:211], v[62:65]
	v_mfma_f32_16x16x32_bf16 v[58:61], v[130:133], v[208:211], v[58:61]
	v_mfma_f32_16x16x32_bf16 v[46:49], v[114:117], v[216:219], v[46:49]
	v_mfma_f32_16x16x32_bf16 v[42:45], v[130:133], v[216:219], v[42:45]
	v_mfma_f32_16x16x32_bf16 v[30:33], v[114:117], v[224:227], v[30:33]
	v_mfma_f32_16x16x32_bf16 v[26:29], v[130:133], v[224:227], v[26:29]
	v_mfma_f32_16x16x32_bf16 v[14:17], v[114:117], v[232:235], v[14:17]
	v_mfma_f32_16x16x32_bf16 v[10:13], v[130:133], v[232:235], v[10:13]
	v_mfma_f32_16x16x32_bf16 v[62:65], v[118:121], v[212:215], v[62:65]
	v_mfma_f32_16x16x32_bf16 v[58:61], v[134:137], v[212:215], v[58:61]
	v_mfma_f32_16x16x32_bf16 v[46:49], v[118:121], v[220:223], v[46:49]
	v_mfma_f32_16x16x32_bf16 v[42:45], v[134:137], v[220:223], v[42:45]
	v_mfma_f32_16x16x32_bf16 v[30:33], v[118:121], v[228:231], v[30:33]
	v_mfma_f32_16x16x32_bf16 v[26:29], v[134:137], v[228:231], v[26:29]
	v_mfma_f32_16x16x32_bf16 v[14:17], v[118:121], v[236:239], v[14:17]
	v_mfma_f32_16x16x32_bf16 v[10:13], v[134:137], v[236:239], v[10:13]
	s_setprio 0
	s_setprio 1
	v_mfma_f32_16x16x32_bf16 v[54:57], v[170:173], v[208:211], v[54:57]
	v_mfma_f32_16x16x32_bf16 v[50:53], v[200:203], v[208:211], v[50:53]
	v_mfma_f32_16x16x32_bf16 v[38:41], v[170:173], v[216:219], v[38:41]
	v_mfma_f32_16x16x32_bf16 v[34:37], v[200:203], v[216:219], v[34:37]
	v_mfma_f32_16x16x32_bf16 v[22:25], v[170:173], v[224:227], v[22:25]
	v_mfma_f32_16x16x32_bf16 v[18:21], v[200:203], v[224:227], v[18:21]
	v_mfma_f32_16x16x32_bf16 v[6:9], v[170:173], v[232:235], v[6:9]
	v_mfma_f32_16x16x32_bf16 v[2:5], v[200:203], v[232:235], v[2:5]
	v_mfma_f32_16x16x32_bf16 v[54:57], v[174:177], v[212:215], v[54:57]
	v_mfma_f32_16x16x32_bf16 v[50:53], v[204:207], v[212:215], v[50:53]
	v_mfma_f32_16x16x32_bf16 v[38:41], v[174:177], v[220:223], v[38:41]
	v_mfma_f32_16x16x32_bf16 v[34:37], v[204:207], v[220:223], v[34:37]
	v_mfma_f32_16x16x32_bf16 v[22:25], v[174:177], v[228:231], v[22:25]
	v_mfma_f32_16x16x32_bf16 v[18:21], v[204:207], v[228:231], v[18:21]
	v_mfma_f32_16x16x32_bf16 v[6:9], v[174:177], v[236:239], v[6:9]
	v_mfma_f32_16x16x32_bf16 v[2:5], v[204:207], v[236:239], v[2:5]
	s_setprio 0
	s_barrier
	s_add_i32 s63, 0, 0x18000
	s_add_i32 s64, 0, 0x1c000
	v_add_u32_e32 v134, s63, v165
	v_add_u32_e32 v162, s64, v165
	ds_read_b128 v[114:117], v134
	ds_read_b128 v[118:121], v134 offset:1024
	ds_read_b128 v[130:133], v134 offset:2048
	ds_read_b128 v[134:137], v134 offset:3072
	ds_read_b128 v[170:173], v162
	ds_read_b128 v[174:177], v162 offset:1024
	ds_read_b128 v[200:203], v162 offset:2048
	ds_read_b128 v[204:207], v162 offset:3072
	s_add_u32 s40, s40, 0x40000
	s_addc_u32 s41, s41, 0
	s_mov_b32 m0, s48
	v_lshl_add_u64 v[244:245], s[40:41], 0, v[146:147]
	ds_read_b128 v[208:211], v168 offset:32768
	ds_read_b128 v[212:215], v168 offset:33792
	ds_read_b128 v[216:219], v168 offset:34816
	ds_read_b128 v[220:223], v168 offset:35840
	ds_read_b128 v[224:227], v168 offset:36864
	ds_read_b128 v[228:231], v168 offset:37888
	ds_read_b128 v[232:235], v168 offset:38912
	ds_read_b128 v[236:239], v168 offset:39936
	global_load_lds_dwordx4 v[244:245], off
	v_lshl_add_u64 v[244:245], s[40:41], 0, v[148:149]
	s_mov_b32 m0, s49
	s_nop 0
	global_load_lds_dwordx4 v[244:245], off
	s_waitcnt vmcnt(8)
	s_waitcnt lgkmcnt(0)
	s_setprio 1
	s_barrier
	v_mfma_f32_16x16x32_bf16 v[142:145], v[114:117], v[208:211], v[142:145]
	v_mfma_f32_16x16x32_bf16 v[138:141], v[130:133], v[208:211], v[138:141]
	v_mfma_f32_16x16x32_bf16 v[110:113], v[114:117], v[216:219], v[110:113]
	v_mfma_f32_16x16x32_bf16 v[106:109], v[130:133], v[216:219], v[106:109]
	v_mfma_f32_16x16x32_bf16 v[94:97], v[114:117], v[224:227], v[94:97]
	v_mfma_f32_16x16x32_bf16 v[90:93], v[130:133], v[224:227], v[90:93]
	v_mfma_f32_16x16x32_bf16 v[78:81], v[114:117], v[232:235], v[78:81]
	v_mfma_f32_16x16x32_bf16 v[74:77], v[130:133], v[232:235], v[74:77]
	v_mfma_f32_16x16x32_bf16 v[142:145], v[118:121], v[212:215], v[142:145]
	v_mfma_f32_16x16x32_bf16 v[138:141], v[134:137], v[212:215], v[138:141]
	v_mfma_f32_16x16x32_bf16 v[110:113], v[118:121], v[220:223], v[110:113]
	v_mfma_f32_16x16x32_bf16 v[106:109], v[134:137], v[220:223], v[106:109]
	v_mfma_f32_16x16x32_bf16 v[94:97], v[118:121], v[228:231], v[94:97]
	v_mfma_f32_16x16x32_bf16 v[90:93], v[134:137], v[228:231], v[90:93]
	v_mfma_f32_16x16x32_bf16 v[78:81], v[118:121], v[236:239], v[78:81]
	v_mfma_f32_16x16x32_bf16 v[74:77], v[134:137], v[236:239], v[74:77]
	s_setprio 0
	s_setprio 1
	v_mfma_f32_16x16x32_bf16 v[126:129], v[170:173], v[208:211], v[126:129]
	v_mfma_f32_16x16x32_bf16 v[122:125], v[200:203], v[208:211], v[122:125]
	v_mfma_f32_16x16x32_bf16 v[102:105], v[170:173], v[216:219], v[102:105]
	v_mfma_f32_16x16x32_bf16 v[98:101], v[200:203], v[216:219], v[98:101]
	v_mfma_f32_16x16x32_bf16 v[86:89], v[170:173], v[224:227], v[86:89]
	v_mfma_f32_16x16x32_bf16 v[82:85], v[200:203], v[224:227], v[82:85]
	v_mfma_f32_16x16x32_bf16 v[70:73], v[170:173], v[232:235], v[70:73]
	v_mfma_f32_16x16x32_bf16 v[66:69], v[200:203], v[232:235], v[66:69]
	v_mfma_f32_16x16x32_bf16 v[126:129], v[174:177], v[212:215], v[126:129]
	v_mfma_f32_16x16x32_bf16 v[122:125], v[204:207], v[212:215], v[122:125]
	v_mfma_f32_16x16x32_bf16 v[102:105], v[174:177], v[220:223], v[102:105]
	v_mfma_f32_16x16x32_bf16 v[98:101], v[204:207], v[220:223], v[98:101]
	v_mfma_f32_16x16x32_bf16 v[86:89], v[174:177], v[228:231], v[86:89]
	v_mfma_f32_16x16x32_bf16 v[82:85], v[204:207], v[228:231], v[82:85]
	v_mfma_f32_16x16x32_bf16 v[70:73], v[174:177], v[236:239], v[70:73]
	v_mfma_f32_16x16x32_bf16 v[66:69], v[204:207], v[236:239], v[66:69]
	s_setprio 0
	s_barrier
	s_add_i32 s40, s63, s42
	v_lshl_add_u64 v[160:161], v[160:161], 0, s[90:91]
	s_mov_b32 m0, s40
	ds_read_b128 v[208:211], v168 offset:49152
	ds_read_b128 v[212:215], v168 offset:50176
	ds_read_b128 v[216:219], v168 offset:51200
	ds_read_b128 v[220:223], v168 offset:52224
	ds_read_b128 v[224:227], v168 offset:53248
	ds_read_b128 v[228:231], v168 offset:54272
	ds_read_b128 v[232:235], v168 offset:55296
	ds_read_b128 v[236:239], v168 offset:56320
	global_load_lds_dwordx4 v[160:161], off
	s_add_i32 m0, s40, 0x2000
	s_add_u32 s38, s38, 0x40080
	v_lshl_add_u64 v[160:161], v[178:179], 0, s[90:91]
	s_addc_u32 s39, s39, 0
	s_add_i32 s40, s64, s42
	global_load_lds_dwordx4 v[160:161], off
	v_lshl_add_u64 v[160:161], s[38:39], 0, v[146:147]
	s_mov_b32 m0, s40
	s_nop 0
	global_load_lds_dwordx4 v[160:161], off
	v_lshl_add_u64 v[160:161], s[38:39], 0, v[148:149]
	s_add_i32 m0, s40, 0x2000
	s_nop 0
	global_load_lds_dwordx4 v[160:161], off
	v_lshl_add_u64 v[160:161], v[240:241], 0, s[90:91]
	s_mov_b32 m0, s52
	s_nop 0
	global_load_lds_dwordx4 v[160:161], off
	v_lshl_add_u64 v[160:161], v[242:243], 0, s[90:91]
	s_mov_b32 m0, s53
	s_nop 0
	global_load_lds_dwordx4 v[160:161], off
	s_waitcnt vmcnt(8)
	s_waitcnt lgkmcnt(0)
	s_setprio 1
	s_barrier
	v_mfma_f32_16x16x32_bf16 v[62:65], v[114:117], v[208:211], v[62:65]
	v_mfma_f32_16x16x32_bf16 v[58:61], v[130:133], v[208:211], v[58:61]
	v_mfma_f32_16x16x32_bf16 v[46:49], v[114:117], v[216:219], v[46:49]
	v_mfma_f32_16x16x32_bf16 v[42:45], v[130:133], v[216:219], v[42:45]
	v_mfma_f32_16x16x32_bf16 v[30:33], v[114:117], v[224:227], v[30:33]
	v_mfma_f32_16x16x32_bf16 v[26:29], v[130:133], v[224:227], v[26:29]
	v_mfma_f32_16x16x32_bf16 v[14:17], v[114:117], v[232:235], v[14:17]
	v_mfma_f32_16x16x32_bf16 v[10:13], v[130:133], v[232:235], v[10:13]
	v_mfma_f32_16x16x32_bf16 v[62:65], v[118:121], v[212:215], v[62:65]
	v_mfma_f32_16x16x32_bf16 v[58:61], v[134:137], v[212:215], v[58:61]
	v_mfma_f32_16x16x32_bf16 v[46:49], v[118:121], v[220:223], v[46:49]
	v_mfma_f32_16x16x32_bf16 v[42:45], v[134:137], v[220:223], v[42:45]
	v_mfma_f32_16x16x32_bf16 v[30:33], v[118:121], v[228:231], v[30:33]
	v_mfma_f32_16x16x32_bf16 v[26:29], v[134:137], v[228:231], v[26:29]
	v_mfma_f32_16x16x32_bf16 v[14:17], v[118:121], v[236:239], v[14:17]
	v_mfma_f32_16x16x32_bf16 v[10:13], v[134:137], v[236:239], v[10:13]
	s_setprio 0
	s_setprio 1
	v_mfma_f32_16x16x32_bf16 v[54:57], v[170:173], v[208:211], v[54:57]
	v_mfma_f32_16x16x32_bf16 v[50:53], v[200:203], v[208:211], v[50:53]
	v_mfma_f32_16x16x32_bf16 v[38:41], v[170:173], v[216:219], v[38:41]
	v_mfma_f32_16x16x32_bf16 v[34:37], v[200:203], v[216:219], v[34:37]
	v_mfma_f32_16x16x32_bf16 v[22:25], v[170:173], v[224:227], v[22:25]
	v_mfma_f32_16x16x32_bf16 v[18:21], v[200:203], v[224:227], v[18:21]
	v_mfma_f32_16x16x32_bf16 v[6:9], v[170:173], v[232:235], v[6:9]
	v_mfma_f32_16x16x32_bf16 v[2:5], v[200:203], v[232:235], v[2:5]
	v_mfma_f32_16x16x32_bf16 v[54:57], v[174:177], v[212:215], v[54:57]
	v_mfma_f32_16x16x32_bf16 v[50:53], v[204:207], v[212:215], v[50:53]
	v_mfma_f32_16x16x32_bf16 v[38:41], v[174:177], v[220:223], v[38:41]
	v_mfma_f32_16x16x32_bf16 v[34:37], v[204:207], v[220:223], v[34:37]
	v_mfma_f32_16x16x32_bf16 v[22:25], v[174:177], v[228:231], v[22:25]
	v_mfma_f32_16x16x32_bf16 v[18:21], v[204:207], v[228:231], v[18:21]
	v_mfma_f32_16x16x32_bf16 v[6:9], v[174:177], v[236:239], v[6:9]
	v_mfma_f32_16x16x32_bf16 v[2:5], v[204:207], v[236:239], v[2:5]
	s_setprio 0
	s_barrier
	s_add_i32 s62, s62, 2
	s_add_u32 s60, s60, 0x100
	s_addc_u32 s61, s61, 0
	s_add_u32 s0, s0, 0x100
	s_addc_u32 s1, s1, 0
	s_cmp_lt_u32 s62, 14
	s_cbranch_scc1 .LBB0_234
	s_andn2_b64 vcc, exec, s[22:23]
	s_cbranch_vccnz .LBB0_237
	s_barrier

.LBB0_318:
	s_add_u32 s41, s10, s40
	s_addc_u32 s42, s11, 0
	s_add_u32 s43, s41, 0x100
	s_addc_u32 s44, s42, 0
	s_and_b64 s[24:25], s[22:23], exec
	s_cselect_b32 s25, s15, s44
	s_cselect_b32 s24, s39, s43
	s_add_u32 s40, s8, s40
	s_addc_u32 s43, s9, 0
	s_add_u32 s40, s40, 0x100
	s_addc_u32 s43, s43, 0
	s_add_i32 s44, 0, 0x10000
	s_and_b64 s[22:23], s[22:23], exec
	v_add_u32_e32 v141, s44, v139
	s_cselect_b32 s23, s17, s43
	s_cselect_b32 s22, s16, s40
	s_add_i32 s43, 0, 0x14000
	ds_read_b128 v[142:145], v141
	ds_read_b128 v[146:149], v141 offset:1024
	ds_read_b128 v[150:153], v141 offset:2048
	ds_read_b128 v[154:157], v141 offset:3072
	v_add_u32_e32 v141, s43, v139
	ds_read_b128 v[158:161], v141
	ds_read_b128 v[164:167], v141 offset:1024
	ds_read_b128 v[168:171], v141 offset:2048
	ds_read_b128 v[172:175], v141 offset:3072
	s_add_u32 s40, s41, 0x20080
	s_addc_u32 s41, s42, 0
	v_lshl_add_u64 v[228:229], s[40:41], 0, v[130:131]
	s_add_i32 m0, s7, 0xc000
	ds_read_b128 v[176:179], v140
	ds_read_b128 v[200:203], v140 offset:1024
	ds_read_b128 v[204:207], v140 offset:2048
	ds_read_b128 v[208:211], v140 offset:3072
	ds_read_b128 v[212:215], v140 offset:4096
	ds_read_b128 v[216:219], v140 offset:5120
	ds_read_b128 v[220:223], v140 offset:6144
	ds_read_b128 v[224:227], v140 offset:7168
	global_load_lds_dwordx4 v[228:229], off
	v_lshl_add_u64 v[228:229], s[40:41], 0, v[132:133]
	s_add_i32 m0, s7, 0xe000
	s_nop 0
	global_load_lds_dwordx4 v[228:229], off
	s_waitcnt vmcnt(8)
	s_waitcnt lgkmcnt(0)
	s_setprio 1
	s_barrier
	v_mfma_f32_16x16x32_bf16 v[126:129], v[142:145], v[176:179], v[126:129]
	v_mfma_f32_16x16x32_bf16 v[122:125], v[150:153], v[176:179], v[122:125]
	v_mfma_f32_16x16x32_bf16 v[118:121], v[142:145], v[204:207], v[118:121]
	v_mfma_f32_16x16x32_bf16 v[114:117], v[150:153], v[204:207], v[114:117]
	v_mfma_f32_16x16x32_bf16 v[106:109], v[142:145], v[212:215], v[106:109]
	v_mfma_f32_16x16x32_bf16 v[98:101], v[150:153], v[212:215], v[98:101]
	v_mfma_f32_16x16x32_bf16 v[90:93], v[142:145], v[220:223], v[90:93]
	v_mfma_f32_16x16x32_bf16 v[82:85], v[150:153], v[220:223], v[82:85]
	v_mfma_f32_16x16x32_bf16 v[126:129], v[146:149], v[200:203], v[126:129]
	v_mfma_f32_16x16x32_bf16 v[122:125], v[154:157], v[200:203], v[122:125]
	v_mfma_f32_16x16x32_bf16 v[118:121], v[146:149], v[208:211], v[118:121]
	v_mfma_f32_16x16x32_bf16 v[114:117], v[154:157], v[208:211], v[114:117]
	v_mfma_f32_16x16x32_bf16 v[106:109], v[146:149], v[216:219], v[106:109]
	v_mfma_f32_16x16x32_bf16 v[98:101], v[154:157], v[216:219], v[98:101]
	v_mfma_f32_16x16x32_bf16 v[90:93], v[146:149], v[224:227], v[90:93]
	v_mfma_f32_16x16x32_bf16 v[82:85], v[154:157], v[224:227], v[82:85]
	s_setprio 0
	s_setprio 1
	v_mfma_f32_16x16x32_bf16 v[110:113], v[158:161], v[176:179], v[110:113]
	v_mfma_f32_16x16x32_bf16 v[102:105], v[168:171], v[176:179], v[102:105]
	v_mfma_f32_16x16x32_bf16 v[94:97], v[158:161], v[204:207], v[94:97]
	v_mfma_f32_16x16x32_bf16 v[86:89], v[168:171], v[204:207], v[86:89]
	v_mfma_f32_16x16x32_bf16 v[78:81], v[158:161], v[212:215], v[78:81]
	v_mfma_f32_16x16x32_bf16 v[74:77], v[168:171], v[212:215], v[74:77]
	v_mfma_f32_16x16x32_bf16 v[70:73], v[158:161], v[220:223], v[70:73]
	v_mfma_f32_16x16x32_bf16 v[66:69], v[168:171], v[220:223], v[66:69]
	v_mfma_f32_16x16x32_bf16 v[110:113], v[164:167], v[200:203], v[110:113]
	v_mfma_f32_16x16x32_bf16 v[102:105], v[172:175], v[200:203], v[102:105]
	v_mfma_f32_16x16x32_bf16 v[94:97], v[164:167], v[208:211], v[94:97]
	v_mfma_f32_16x16x32_bf16 v[86:89], v[172:175], v[208:211], v[86:89]
	v_mfma_f32_16x16x32_bf16 v[78:81], v[164:167], v[216:219], v[78:81]
	v_mfma_f32_16x16x32_bf16 v[74:77], v[172:175], v[216:219], v[74:77]
	v_mfma_f32_16x16x32_bf16 v[70:73], v[164:167], v[224:227], v[70:73]
	v_mfma_f32_16x16x32_bf16 v[66:69], v[172:175], v[224:227], v[66:69]
	s_setprio 0
	s_barrier
	s_add_i32 s40, s44, s31
	v_lshl_add_u64 v[228:229], s[22:23], 0, v[162:163]
	s_mov_b32 m0, s40
	ds_read_b128 v[176:179], v140 offset:16384
	ds_read_b128 v[200:203], v140 offset:17408
	ds_read_b128 v[204:207], v140 offset:18432
	ds_read_b128 v[208:211], v140 offset:19456
	ds_read_b128 v[212:215], v140 offset:20480
	ds_read_b128 v[216:219], v140 offset:21504
	ds_read_b128 v[220:223], v140 offset:22528
	ds_read_b128 v[224:227], v140 offset:23552
	global_load_lds_dwordx4 v[228:229], off
	s_add_i32 m0, s40, 0x2000
	s_add_u32 s40, s22, 0x10000
	v_lshl_add_u64 v[230:231], s[22:23], 0, v[134:135]
	s_addc_u32 s41, s23, 0
	s_add_i32 s42, s43, s31
	global_load_lds_dwordx4 v[230:231], off
	v_lshl_add_u64 v[232:233], s[40:41], 0, v[162:163]
	s_mov_b32 m0, s42
	v_lshl_add_u64 v[234:235], s[24:25], 0, v[132:133]
	global_load_lds_dwordx4 v[232:233], off
	v_lshl_add_u64 v[232:233], s[40:41], 0, v[134:135]
	s_add_i32 m0, s42, 0x2000
	s_nop 0
	global_load_lds_dwordx4 v[232:233], off
	v_lshl_add_u64 v[232:233], s[24:25], 0, v[130:131]
	s_mov_b32 m0, s7
	s_nop 0
	global_load_lds_dwordx4 v[232:233], off
	s_mov_b32 m0, s33
	s_nop 0
	global_load_lds_dwordx4 v[234:235], off
	s_waitcnt vmcnt(8)
	s_waitcnt lgkmcnt(0)
	s_setprio 1
	s_barrier
	v_mfma_f32_16x16x32_bf16 v[62:65], v[142:145], v[176:179], v[62:65]
	v_mfma_f32_16x16x32_bf16 v[58:61], v[150:153], v[176:179], v[58:61]
	v_mfma_f32_16x16x32_bf16 v[54:57], v[142:145], v[204:207], v[54:57]
	v_mfma_f32_16x16x32_bf16 v[50:53], v[150:153], v[204:207], v[50:53]
	v_mfma_f32_16x16x32_bf16 v[42:45], v[142:145], v[212:215], v[42:45]
	v_mfma_f32_16x16x32_bf16 v[34:37], v[150:153], v[212:215], v[34:37]
	v_mfma_f32_16x16x32_bf16 v[26:29], v[142:145], v[220:223], v[26:29]
	v_mfma_f32_16x16x32_bf16 v[18:21], v[150:153], v[220:223], v[18:21]
	v_mfma_f32_16x16x32_bf16 v[62:65], v[146:149], v[200:203], v[62:65]
	v_mfma_f32_16x16x32_bf16 v[58:61], v[154:157], v[200:203], v[58:61]
	v_mfma_f32_16x16x32_bf16 v[54:57], v[146:149], v[208:211], v[54:57]
	v_mfma_f32_16x16x32_bf16 v[50:53], v[154:157], v[208:211], v[50:53]
	v_mfma_f32_16x16x32_bf16 v[42:45], v[146:149], v[216:219], v[42:45]
	v_mfma_f32_16x16x32_bf16 v[34:37], v[154:157], v[216:219], v[34:37]
	v_mfma_f32_16x16x32_bf16 v[26:29], v[146:149], v[224:227], v[26:29]
	v_mfma_f32_16x16x32_bf16 v[18:21], v[154:157], v[224:227], v[18:21]
	s_setprio 0
	s_setprio 1
	v_mfma_f32_16x16x32_bf16 v[46:49], v[158:161], v[176:179], v[46:49]
	v_mfma_f32_16x16x32_bf16 v[38:41], v[168:171], v[176:179], v[38:41]
	v_mfma_f32_16x16x32_bf16 v[30:33], v[158:161], v[204:207], v[30:33]
	v_mfma_f32_16x16x32_bf16 v[22:25], v[168:171], v[204:207], v[22:25]
	v_mfma_f32_16x16x32_bf16 v[14:17], v[158:161], v[212:215], v[14:17]
	v_mfma_f32_16x16x32_bf16 v[10:13], v[168:171], v[212:215], v[10:13]
	v_mfma_f32_16x16x32_bf16 v[6:9], v[158:161], v[220:223], v[6:9]
	v_mfma_f32_16x16x32_bf16 v[2:5], v[168:171], v[220:223], v[2:5]
	v_mfma_f32_16x16x32_bf16 v[46:49], v[164:167], v[200:203], v[46:49]
	v_mfma_f32_16x16x32_bf16 v[38:41], v[172:175], v[200:203], v[38:41]
	v_mfma_f32_16x16x32_bf16 v[30:33], v[164:167], v[208:211], v[30:33]
	v_mfma_f32_16x16x32_bf16 v[22:25], v[172:175], v[208:211], v[22:25]
	v_mfma_f32_16x16x32_bf16 v[14:17], v[164:167], v[216:219], v[14:17]
	v_mfma_f32_16x16x32_bf16 v[10:13], v[172:175], v[216:219], v[10:13]
	v_mfma_f32_16x16x32_bf16 v[6:9], v[164:167], v[224:227], v[6:9]
	v_mfma_f32_16x16x32_bf16 v[2:5], v[172:175], v[224:227], v[2:5]
	s_setprio 0
	s_barrier
	s_add_i32 s40, 0, 0x18000
	v_add_u32_e32 v141, s40, v139
	s_add_i32 s41, 0, 0x1c000
	ds_read_b128 v[142:145], v141
	ds_read_b128 v[146:149], v141 offset:1024
	ds_read_b128 v[150:153], v141 offset:2048
	ds_read_b128 v[154:157], v141 offset:3072
	v_add_u32_e32 v141, s41, v139
	ds_read_b128 v[158:161], v141
	ds_read_b128 v[164:167], v141 offset:1024
	ds_read_b128 v[168:171], v141 offset:2048
	ds_read_b128 v[172:175], v141 offset:3072
	s_add_u32 s24, s24, 0x20000
	s_addc_u32 s25, s25, 0
	s_mov_b32 m0, s34
	v_lshl_add_u64 v[236:237], s[24:25], 0, v[130:131]
	ds_read_b128 v[176:179], v140 offset:32768
	ds_read_b128 v[200:203], v140 offset:33792
	ds_read_b128 v[204:207], v140 offset:34816
	ds_read_b128 v[208:211], v140 offset:35840
	ds_read_b128 v[212:215], v140 offset:36864
	ds_read_b128 v[216:219], v140 offset:37888
	ds_read_b128 v[220:223], v140 offset:38912
	ds_read_b128 v[224:227], v140 offset:39936
	global_load_lds_dwordx4 v[236:237], off
	v_lshl_add_u64 v[236:237], s[24:25], 0, v[132:133]
	s_mov_b32 m0, s35
	s_nop 0
	global_load_lds_dwordx4 v[236:237], off
	s_waitcnt vmcnt(8)
	s_waitcnt lgkmcnt(0)
	s_setprio 1
	s_barrier
	v_mfma_f32_16x16x32_bf16 v[126:129], v[142:145], v[176:179], v[126:129]
	v_mfma_f32_16x16x32_bf16 v[122:125], v[150:153], v[176:179], v[122:125]
	v_mfma_f32_16x16x32_bf16 v[118:121], v[142:145], v[204:207], v[118:121]
	v_mfma_f32_16x16x32_bf16 v[114:117], v[150:153], v[204:207], v[114:117]
	v_mfma_f32_16x16x32_bf16 v[106:109], v[142:145], v[212:215], v[106:109]
	v_mfma_f32_16x16x32_bf16 v[98:101], v[150:153], v[212:215], v[98:101]
	v_mfma_f32_16x16x32_bf16 v[90:93], v[142:145], v[220:223], v[90:93]
	v_mfma_f32_16x16x32_bf16 v[82:85], v[150:153], v[220:223], v[82:85]
	v_mfma_f32_16x16x32_bf16 v[126:129], v[146:149], v[200:203], v[126:129]
	v_mfma_f32_16x16x32_bf16 v[122:125], v[154:157], v[200:203], v[122:125]
	v_mfma_f32_16x16x32_bf16 v[118:121], v[146:149], v[208:211], v[118:121]
	v_mfma_f32_16x16x32_bf16 v[114:117], v[154:157], v[208:211], v[114:117]
	v_mfma_f32_16x16x32_bf16 v[106:109], v[146:149], v[216:219], v[106:109]
	v_mfma_f32_16x16x32_bf16 v[98:101], v[154:157], v[216:219], v[98:101]
	v_mfma_f32_16x16x32_bf16 v[90:93], v[146:149], v[224:227], v[90:93]
	v_mfma_f32_16x16x32_bf16 v[82:85], v[154:157], v[224:227], v[82:85]
	s_setprio 0
	s_setprio 1
	v_mfma_f32_16x16x32_bf16 v[110:113], v[158:161], v[176:179], v[110:113]
	v_mfma_f32_16x16x32_bf16 v[102:105], v[168:171], v[176:179], v[102:105]
	v_mfma_f32_16x16x32_bf16 v[94:97], v[158:161], v[204:207], v[94:97]
	v_mfma_f32_16x16x32_bf16 v[86:89], v[168:171], v[204:207], v[86:89]
	v_mfma_f32_16x16x32_bf16 v[78:81], v[158:161], v[212:215], v[78:81]
	v_mfma_f32_16x16x32_bf16 v[74:77], v[168:171], v[212:215], v[74:77]
	v_mfma_f32_16x16x32_bf16 v[70:73], v[158:161], v[220:223], v[70:73]
	v_mfma_f32_16x16x32_bf16 v[66:69], v[168:171], v[220:223], v[66:69]
	v_mfma_f32_16x16x32_bf16 v[110:113], v[164:167], v[200:203], v[110:113]
	v_mfma_f32_16x16x32_bf16 v[102:105], v[172:175], v[200:203], v[102:105]
	v_mfma_f32_16x16x32_bf16 v[94:97], v[164:167], v[208:211], v[94:97]
	v_mfma_f32_16x16x32_bf16 v[86:89], v[172:175], v[208:211], v[86:89]
	v_mfma_f32_16x16x32_bf16 v[78:81], v[164:167], v[216:219], v[78:81]
	v_mfma_f32_16x16x32_bf16 v[74:77], v[172:175], v[216:219], v[74:77]
	v_mfma_f32_16x16x32_bf16 v[70:73], v[164:167], v[224:227], v[70:73]
	v_mfma_f32_16x16x32_bf16 v[66:69], v[172:175], v[224:227], v[66:69]
	s_setprio 0
	s_barrier
	s_add_i32 s24, s40, s31
	v_lshl_add_u64 v[228:229], v[228:229], 0, s[90:91]
	s_mov_b32 m0, s24
	ds_read_b128 v[176:179], v140 offset:49152
	ds_read_b128 v[200:203], v140 offset:50176
	ds_read_b128 v[204:207], v140 offset:51200
	ds_read_b128 v[208:211], v140 offset:52224
	ds_read_b128 v[212:215], v140 offset:53248
	ds_read_b128 v[216:219], v140 offset:54272
	ds_read_b128 v[220:223], v140 offset:55296
	ds_read_b128 v[224:227], v140 offset:56320
	global_load_lds_dwordx4 v[228:229], off
	s_add_i32 m0, s24, 0x2000
	s_add_u32 s22, s22, 0x10080
	v_lshl_add_u64 v[228:229], v[230:231], 0, s[90:91]
	s_addc_u32 s23, s23, 0
	s_add_i32 s24, s41, s31
	global_load_lds_dwordx4 v[228:229], off
	v_lshl_add_u64 v[228:229], s[22:23], 0, v[162:163]
	s_mov_b32 m0, s24
	s_nop 0
	global_load_lds_dwordx4 v[228:229], off
	v_lshl_add_u64 v[228:229], s[22:23], 0, v[134:135]
	s_add_i32 m0, s24, 0x2000
	s_nop 0
	global_load_lds_dwordx4 v[228:229], off
	v_lshl_add_u64 v[228:229], v[232:233], 0, s[90:91]
	s_mov_b32 m0, s36
	s_nop 0
	global_load_lds_dwordx4 v[228:229], off
	v_lshl_add_u64 v[228:229], v[234:235], 0, s[90:91]
	s_mov_b32 m0, s37
	s_nop 0
	global_load_lds_dwordx4 v[228:229], off
	s_waitcnt vmcnt(8)
	s_waitcnt lgkmcnt(0)
	s_setprio 1
	s_barrier
	v_mfma_f32_16x16x32_bf16 v[62:65], v[142:145], v[176:179], v[62:65]
	v_mfma_f32_16x16x32_bf16 v[58:61], v[150:153], v[176:179], v[58:61]
	v_mfma_f32_16x16x32_bf16 v[54:57], v[142:145], v[204:207], v[54:57]
	v_mfma_f32_16x16x32_bf16 v[50:53], v[150:153], v[204:207], v[50:53]
	v_mfma_f32_16x16x32_bf16 v[42:45], v[142:145], v[212:215], v[42:45]
	v_mfma_f32_16x16x32_bf16 v[34:37], v[150:153], v[212:215], v[34:37]
	v_mfma_f32_16x16x32_bf16 v[26:29], v[142:145], v[220:223], v[26:29]
	v_mfma_f32_16x16x32_bf16 v[18:21], v[150:153], v[220:223], v[18:21]
	v_mfma_f32_16x16x32_bf16 v[62:65], v[146:149], v[200:203], v[62:65]
	v_mfma_f32_16x16x32_bf16 v[58:61], v[154:157], v[200:203], v[58:61]
	v_mfma_f32_16x16x32_bf16 v[54:57], v[146:149], v[208:211], v[54:57]
	v_mfma_f32_16x16x32_bf16 v[50:53], v[154:157], v[208:211], v[50:53]
	v_mfma_f32_16x16x32_bf16 v[42:45], v[146:149], v[216:219], v[42:45]
	v_mfma_f32_16x16x32_bf16 v[34:37], v[154:157], v[216:219], v[34:37]
	v_mfma_f32_16x16x32_bf16 v[26:29], v[146:149], v[224:227], v[26:29]
	v_mfma_f32_16x16x32_bf16 v[18:21], v[154:157], v[224:227], v[18:21]
	s_setprio 0
	s_setprio 1
	v_mfma_f32_16x16x32_bf16 v[46:49], v[158:161], v[176:179], v[46:49]
	v_mfma_f32_16x16x32_bf16 v[38:41], v[168:171], v[176:179], v[38:41]
	v_mfma_f32_16x16x32_bf16 v[30:33], v[158:161], v[204:207], v[30:33]
	v_mfma_f32_16x16x32_bf16 v[22:25], v[168:171], v[204:207], v[22:25]
	v_mfma_f32_16x16x32_bf16 v[14:17], v[158:161], v[212:215], v[14:17]
	v_mfma_f32_16x16x32_bf16 v[10:13], v[168:171], v[212:215], v[10:13]
	v_mfma_f32_16x16x32_bf16 v[6:9], v[158:161], v[220:223], v[6:9]
	v_mfma_f32_16x16x32_bf16 v[2:5], v[168:171], v[220:223], v[2:5]
	v_mfma_f32_16x16x32_bf16 v[46:49], v[164:167], v[200:203], v[46:49]
	v_mfma_f32_16x16x32_bf16 v[38:41], v[172:175], v[200:203], v[38:41]
	v_mfma_f32_16x16x32_bf16 v[30:33], v[164:167], v[208:211], v[30:33]
	v_mfma_f32_16x16x32_bf16 v[22:25], v[172:175], v[208:211], v[22:25]
	v_mfma_f32_16x16x32_bf16 v[14:17], v[164:167], v[216:219], v[14:17]
	v_mfma_f32_16x16x32_bf16 v[10:13], v[172:175], v[216:219], v[10:13]
	v_mfma_f32_16x16x32_bf16 v[6:9], v[164:167], v[224:227], v[6:9]
	v_mfma_f32_16x16x32_bf16 v[2:5], v[172:175], v[224:227], v[2:5]
	s_setprio 0
	s_barrier
	s_movk_i32 s40, 0x100
	s_and_b64 vcc, exec, s[20:21]
	s_mov_b64 s[22:23], -1
	s_mov_b64 s[20:21], 0
	s_cbranch_vccnz .LBB0_318
	s_andn2_b64 vcc, exec, s[12:13]
	s_cbranch_vccnz .LBB0_321
	s_barrier

.LBB0_775:
	s_add_u32 s20, s18, 0xfffe0080
	s_addc_u32 s21, s19, -1
	s_add_i32 s42, 0, 0x10000
	s_cmp_eq_u32 s41, 4
	s_cselect_b32 s23, s11, s21
	s_cselect_b32 s22, s17, s20
	v_add_u32_e32 v139, s42, v141
	s_cselect_b32 s21, s13, s40
	s_cselect_b32 s20, s12, s33
	s_add_i32 s44, 0, 0x14000
	ds_read_b128 v[146:149], v139
	ds_read_b128 v[150:153], v139 offset:1024
	ds_read_b128 v[154:157], v139 offset:2048
	ds_read_b128 v[158:161], v139 offset:3072
	v_add_u32_e32 v139, s44, v141
	ds_read_b128 v[164:167], v139
	ds_read_b128 v[172:175], v139 offset:1024
	ds_read_b128 v[176:179], v139 offset:2048
	ds_read_b128 v[200:203], v139 offset:3072
	v_lshl_add_u64 v[168:169], s[18:19], 0, v[136:137]
	s_add_i32 m0, s30, 0xc000
	ds_read_b128 v[204:207], v144
	ds_read_b128 v[208:211], v144 offset:1024
	ds_read_b128 v[212:215], v144 offset:2048
	ds_read_b128 v[216:219], v144 offset:3072
	ds_read_b128 v[220:223], v144 offset:4096
	ds_read_b128 v[224:227], v144 offset:5120
	ds_read_b128 v[228:231], v144 offset:6144
	ds_read_b128 v[232:235], v144 offset:7168
	global_load_lds_dwordx4 v[168:169], off
	v_lshl_add_u64 v[168:169], s[18:19], 0, v[134:135]
	s_add_i32 m0, s30, 0xe000
	s_nop 0
	global_load_lds_dwordx4 v[168:169], off
	s_waitcnt vmcnt(8)
	s_waitcnt lgkmcnt(0)
	s_setprio 1
	s_barrier
	v_mfma_f32_16x16x32_bf16 v[126:129], v[146:149], v[204:207], v[126:129]
	v_mfma_f32_16x16x32_bf16 v[122:125], v[154:157], v[204:207], v[122:125]
	v_mfma_f32_16x16x32_bf16 v[110:113], v[146:149], v[212:215], v[110:113]
	v_mfma_f32_16x16x32_bf16 v[106:109], v[154:157], v[212:215], v[106:109]
	v_mfma_f32_16x16x32_bf16 v[94:97], v[146:149], v[220:223], v[94:97]
	v_mfma_f32_16x16x32_bf16 v[90:93], v[154:157], v[220:223], v[90:93]
	v_mfma_f32_16x16x32_bf16 v[78:81], v[146:149], v[228:231], v[78:81]
	v_mfma_f32_16x16x32_bf16 v[74:77], v[154:157], v[228:231], v[74:77]
	v_mfma_f32_16x16x32_bf16 v[126:129], v[150:153], v[208:211], v[126:129]
	v_mfma_f32_16x16x32_bf16 v[122:125], v[158:161], v[208:211], v[122:125]
	v_mfma_f32_16x16x32_bf16 v[110:113], v[150:153], v[216:219], v[110:113]
	v_mfma_f32_16x16x32_bf16 v[106:109], v[158:161], v[216:219], v[106:109]
	v_mfma_f32_16x16x32_bf16 v[94:97], v[150:153], v[224:227], v[94:97]
	v_mfma_f32_16x16x32_bf16 v[90:93], v[158:161], v[224:227], v[90:93]
	v_mfma_f32_16x16x32_bf16 v[78:81], v[150:153], v[232:235], v[78:81]
	v_mfma_f32_16x16x32_bf16 v[74:77], v[158:161], v[232:235], v[74:77]
	s_setprio 0
	s_setprio 1
	v_mfma_f32_16x16x32_bf16 v[118:121], v[164:167], v[204:207], v[118:121]
	v_mfma_f32_16x16x32_bf16 v[114:117], v[176:179], v[204:207], v[114:117]
	v_mfma_f32_16x16x32_bf16 v[102:105], v[164:167], v[212:215], v[102:105]
	v_mfma_f32_16x16x32_bf16 v[98:101], v[176:179], v[212:215], v[98:101]
	v_mfma_f32_16x16x32_bf16 v[86:89], v[164:167], v[220:223], v[86:89]
	v_mfma_f32_16x16x32_bf16 v[82:85], v[176:179], v[220:223], v[82:85]
	v_mfma_f32_16x16x32_bf16 v[70:73], v[164:167], v[228:231], v[70:73]
	v_mfma_f32_16x16x32_bf16 v[66:69], v[176:179], v[228:231], v[66:69]
	v_mfma_f32_16x16x32_bf16 v[118:121], v[172:175], v[208:211], v[118:121]
	v_mfma_f32_16x16x32_bf16 v[114:117], v[200:203], v[208:211], v[114:117]
	v_mfma_f32_16x16x32_bf16 v[102:105], v[172:175], v[216:219], v[102:105]
	v_mfma_f32_16x16x32_bf16 v[98:101], v[200:203], v[216:219], v[98:101]
	v_mfma_f32_16x16x32_bf16 v[86:89], v[172:175], v[224:227], v[86:89]
	v_mfma_f32_16x16x32_bf16 v[82:85], v[200:203], v[224:227], v[82:85]
	v_mfma_f32_16x16x32_bf16 v[70:73], v[172:175], v[232:235], v[70:73]
	v_mfma_f32_16x16x32_bf16 v[66:69], v[200:203], v[232:235], v[66:69]
	s_setprio 0
	s_barrier
	s_add_i32 s42, s42, s29
	v_lshl_add_u64 v[168:169], s[20:21], 0, v[130:131]
	s_mov_b32 m0, s42
	ds_read_b128 v[204:207], v144 offset:16384
	ds_read_b128 v[208:211], v144 offset:17408
	ds_read_b128 v[212:215], v144 offset:18432
	ds_read_b128 v[216:219], v144 offset:19456
	ds_read_b128 v[220:223], v144 offset:20480
	ds_read_b128 v[224:227], v144 offset:21504
	ds_read_b128 v[228:231], v144 offset:22528
	ds_read_b128 v[232:235], v144 offset:23552
	global_load_lds_dwordx4 v[168:169], off
	s_add_i32 m0, s42, 0x2000
	s_add_u32 s42, s20, 0x20000
	v_lshl_add_u64 v[236:237], s[20:21], 0, v[132:133]
	s_addc_u32 s43, s21, 0
	s_add_i32 s44, s44, s29
	global_load_lds_dwordx4 v[236:237], off
	v_lshl_add_u64 v[238:239], s[42:43], 0, v[130:131]
	s_mov_b32 m0, s44
	v_lshl_add_u64 v[240:241], s[22:23], 0, v[132:133]
	global_load_lds_dwordx4 v[238:239], off
	v_lshl_add_u64 v[238:239], s[42:43], 0, v[132:133]
	s_add_i32 m0, s44, 0x2000
	s_nop 0
	global_load_lds_dwordx4 v[238:239], off
	v_lshl_add_u64 v[238:239], s[22:23], 0, v[130:131]
	s_mov_b32 m0, s30
	s_nop 0
	global_load_lds_dwordx4 v[238:239], off
	s_mov_b32 m0, s31
	s_nop 0
	global_load_lds_dwordx4 v[240:241], off
	s_waitcnt vmcnt(8)
	s_waitcnt lgkmcnt(0)
	s_setprio 1
	s_barrier
	v_mfma_f32_16x16x32_bf16 v[62:65], v[146:149], v[204:207], v[62:65]
	v_mfma_f32_16x16x32_bf16 v[58:61], v[154:157], v[204:207], v[58:61]
	v_mfma_f32_16x16x32_bf16 v[46:49], v[146:149], v[212:215], v[46:49]
	v_mfma_f32_16x16x32_bf16 v[42:45], v[154:157], v[212:215], v[42:45]
	v_mfma_f32_16x16x32_bf16 v[30:33], v[146:149], v[220:223], v[30:33]
	v_mfma_f32_16x16x32_bf16 v[26:29], v[154:157], v[220:223], v[26:29]
	v_mfma_f32_16x16x32_bf16 v[14:17], v[146:149], v[228:231], v[14:17]
	v_mfma_f32_16x16x32_bf16 v[10:13], v[154:157], v[228:231], v[10:13]
	v_mfma_f32_16x16x32_bf16 v[62:65], v[150:153], v[208:211], v[62:65]
	v_mfma_f32_16x16x32_bf16 v[58:61], v[158:161], v[208:211], v[58:61]
	v_mfma_f32_16x16x32_bf16 v[46:49], v[150:153], v[216:219], v[46:49]
	v_mfma_f32_16x16x32_bf16 v[42:45], v[158:161], v[216:219], v[42:45]
	v_mfma_f32_16x16x32_bf16 v[30:33], v[150:153], v[224:227], v[30:33]
	v_mfma_f32_16x16x32_bf16 v[26:29], v[158:161], v[224:227], v[26:29]
	v_mfma_f32_16x16x32_bf16 v[14:17], v[150:153], v[232:235], v[14:17]
	v_mfma_f32_16x16x32_bf16 v[10:13], v[158:161], v[232:235], v[10:13]
	s_setprio 0
	s_setprio 1
	v_mfma_f32_16x16x32_bf16 v[54:57], v[164:167], v[204:207], v[54:57]
	v_mfma_f32_16x16x32_bf16 v[50:53], v[176:179], v[204:207], v[50:53]
	v_mfma_f32_16x16x32_bf16 v[38:41], v[164:167], v[212:215], v[38:41]
	v_mfma_f32_16x16x32_bf16 v[34:37], v[176:179], v[212:215], v[34:37]
	v_mfma_f32_16x16x32_bf16 v[22:25], v[164:167], v[220:223], v[22:25]
	v_mfma_f32_16x16x32_bf16 v[18:21], v[176:179], v[220:223], v[18:21]
	v_mfma_f32_16x16x32_bf16 v[6:9], v[164:167], v[228:231], v[6:9]
	v_mfma_f32_16x16x32_bf16 v[2:5], v[176:179], v[228:231], v[2:5]
	v_mfma_f32_16x16x32_bf16 v[54:57], v[172:175], v[208:211], v[54:57]
	v_mfma_f32_16x16x32_bf16 v[50:53], v[200:203], v[208:211], v[50:53]
	v_mfma_f32_16x16x32_bf16 v[38:41], v[172:175], v[216:219], v[38:41]
	v_mfma_f32_16x16x32_bf16 v[34:37], v[200:203], v[216:219], v[34:37]
	v_mfma_f32_16x16x32_bf16 v[22:25], v[172:175], v[224:227], v[22:25]
	v_mfma_f32_16x16x32_bf16 v[18:21], v[200:203], v[224:227], v[18:21]
	v_mfma_f32_16x16x32_bf16 v[6:9], v[172:175], v[232:235], v[6:9]
	v_mfma_f32_16x16x32_bf16 v[2:5], v[200:203], v[232:235], v[2:5]
	s_setprio 0
	s_barrier
	s_add_i32 s42, 0, 0x18000
	v_add_u32_e32 v139, s42, v141
	s_add_i32 s43, 0, 0x1c000
	ds_read_b128 v[146:149], v139
	ds_read_b128 v[150:153], v139 offset:1024
	ds_read_b128 v[154:157], v139 offset:2048
	ds_read_b128 v[158:161], v139 offset:3072
	v_add_u32_e32 v139, s43, v141
	ds_read_b128 v[164:167], v139
	ds_read_b128 v[172:175], v139 offset:1024
	ds_read_b128 v[176:179], v139 offset:2048
	ds_read_b128 v[200:203], v139 offset:3072
	s_add_u32 s22, s22, 0x20000
	s_addc_u32 s23, s23, 0
	s_mov_b32 m0, s34
	v_lshl_add_u64 v[242:243], s[22:23], 0, v[130:131]
	ds_read_b128 v[204:207], v144 offset:32768
	ds_read_b128 v[208:211], v144 offset:33792
	ds_read_b128 v[212:215], v144 offset:34816
	ds_read_b128 v[216:219], v144 offset:35840
	ds_read_b128 v[220:223], v144 offset:36864
	ds_read_b128 v[224:227], v144 offset:37888
	ds_read_b128 v[228:231], v144 offset:38912
	ds_read_b128 v[232:235], v144 offset:39936
	global_load_lds_dwordx4 v[242:243], off
	v_lshl_add_u64 v[242:243], s[22:23], 0, v[132:133]
	s_mov_b32 m0, s35
	s_nop 0
	global_load_lds_dwordx4 v[242:243], off
	s_waitcnt vmcnt(8)
	s_waitcnt lgkmcnt(0)
	s_setprio 1
	s_barrier
	v_mfma_f32_16x16x32_bf16 v[126:129], v[146:149], v[204:207], v[126:129]
	v_mfma_f32_16x16x32_bf16 v[122:125], v[154:157], v[204:207], v[122:125]
	v_mfma_f32_16x16x32_bf16 v[110:113], v[146:149], v[212:215], v[110:113]
	v_mfma_f32_16x16x32_bf16 v[106:109], v[154:157], v[212:215], v[106:109]
	v_mfma_f32_16x16x32_bf16 v[94:97], v[146:149], v[220:223], v[94:97]
	v_mfma_f32_16x16x32_bf16 v[90:93], v[154:157], v[220:223], v[90:93]
	v_mfma_f32_16x16x32_bf16 v[78:81], v[146:149], v[228:231], v[78:81]
	v_mfma_f32_16x16x32_bf16 v[74:77], v[154:157], v[228:231], v[74:77]
	v_mfma_f32_16x16x32_bf16 v[126:129], v[150:153], v[208:211], v[126:129]
	v_mfma_f32_16x16x32_bf16 v[122:125], v[158:161], v[208:211], v[122:125]
	v_mfma_f32_16x16x32_bf16 v[110:113], v[150:153], v[216:219], v[110:113]
	v_mfma_f32_16x16x32_bf16 v[106:109], v[158:161], v[216:219], v[106:109]
	v_mfma_f32_16x16x32_bf16 v[94:97], v[150:153], v[224:227], v[94:97]
	v_mfma_f32_16x16x32_bf16 v[90:93], v[158:161], v[224:227], v[90:93]
	v_mfma_f32_16x16x32_bf16 v[78:81], v[150:153], v[232:235], v[78:81]
	v_mfma_f32_16x16x32_bf16 v[74:77], v[158:161], v[232:235], v[74:77]
	s_setprio 0
	s_setprio 1
	v_mfma_f32_16x16x32_bf16 v[118:121], v[164:167], v[204:207], v[118:121]
	v_mfma_f32_16x16x32_bf16 v[114:117], v[176:179], v[204:207], v[114:117]
	v_mfma_f32_16x16x32_bf16 v[102:105], v[164:167], v[212:215], v[102:105]
	v_mfma_f32_16x16x32_bf16 v[98:101], v[176:179], v[212:215], v[98:101]
	v_mfma_f32_16x16x32_bf16 v[86:89], v[164:167], v[220:223], v[86:89]
	v_mfma_f32_16x16x32_bf16 v[82:85], v[176:179], v[220:223], v[82:85]
	v_mfma_f32_16x16x32_bf16 v[70:73], v[164:167], v[228:231], v[70:73]
	v_mfma_f32_16x16x32_bf16 v[66:69], v[176:179], v[228:231], v[66:69]
	v_mfma_f32_16x16x32_bf16 v[118:121], v[172:175], v[208:211], v[118:121]
	v_mfma_f32_16x16x32_bf16 v[114:117], v[200:203], v[208:211], v[114:117]
	v_mfma_f32_16x16x32_bf16 v[102:105], v[172:175], v[216:219], v[102:105]
	v_mfma_f32_16x16x32_bf16 v[98:101], v[200:203], v[216:219], v[98:101]
	v_mfma_f32_16x16x32_bf16 v[86:89], v[172:175], v[224:227], v[86:89]
	v_mfma_f32_16x16x32_bf16 v[82:85], v[200:203], v[224:227], v[82:85]
	v_mfma_f32_16x16x32_bf16 v[70:73], v[172:175], v[232:235], v[70:73]
	v_mfma_f32_16x16x32_bf16 v[66:69], v[200:203], v[232:235], v[66:69]
	s_setprio 0
	s_barrier
	s_add_i32 s22, s42, s29
	v_lshl_add_u64 v[168:169], v[168:169], 0, s[90:91]
	s_mov_b32 m0, s22
	ds_read_b128 v[204:207], v144 offset:49152
	ds_read_b128 v[208:211], v144 offset:50176
	ds_read_b128 v[212:215], v144 offset:51200
	ds_read_b128 v[216:219], v144 offset:52224
	ds_read_b128 v[220:223], v144 offset:53248
	ds_read_b128 v[224:227], v144 offset:54272
	ds_read_b128 v[228:231], v144 offset:55296
	ds_read_b128 v[232:235], v144 offset:56320
	global_load_lds_dwordx4 v[168:169], off
	s_add_i32 m0, s22, 0x2000
	s_add_u32 s20, s20, 0x20080
	v_lshl_add_u64 v[168:169], v[236:237], 0, s[90:91]
	s_addc_u32 s21, s21, 0
	s_add_i32 s22, s43, s29
	global_load_lds_dwordx4 v[168:169], off
	v_lshl_add_u64 v[168:169], s[20:21], 0, v[130:131]
	s_mov_b32 m0, s22
	s_nop 0
	global_load_lds_dwordx4 v[168:169], off
	v_lshl_add_u64 v[168:169], s[20:21], 0, v[132:133]
	s_add_i32 m0, s22, 0x2000
	s_nop 0
	global_load_lds_dwordx4 v[168:169], off
	v_lshl_add_u64 v[168:169], v[238:239], 0, s[90:91]
	s_mov_b32 m0, s37
	s_nop 0
	global_load_lds_dwordx4 v[168:169], off
	v_lshl_add_u64 v[168:169], v[240:241], 0, s[90:91]
	s_mov_b32 m0, s38
	s_nop 0
	global_load_lds_dwordx4 v[168:169], off
	s_waitcnt vmcnt(8)
	s_waitcnt lgkmcnt(0)
	s_setprio 1
	s_barrier
	v_mfma_f32_16x16x32_bf16 v[62:65], v[146:149], v[204:207], v[62:65]
	v_mfma_f32_16x16x32_bf16 v[58:61], v[154:157], v[204:207], v[58:61]
	v_mfma_f32_16x16x32_bf16 v[46:49], v[146:149], v[212:215], v[46:49]
	v_mfma_f32_16x16x32_bf16 v[42:45], v[154:157], v[212:215], v[42:45]
	v_mfma_f32_16x16x32_bf16 v[30:33], v[146:149], v[220:223], v[30:33]
	v_mfma_f32_16x16x32_bf16 v[26:29], v[154:157], v[220:223], v[26:29]
	v_mfma_f32_16x16x32_bf16 v[14:17], v[146:149], v[228:231], v[14:17]
	v_mfma_f32_16x16x32_bf16 v[10:13], v[154:157], v[228:231], v[10:13]
	v_mfma_f32_16x16x32_bf16 v[62:65], v[150:153], v[208:211], v[62:65]
	v_mfma_f32_16x16x32_bf16 v[58:61], v[158:161], v[208:211], v[58:61]
	v_mfma_f32_16x16x32_bf16 v[46:49], v[150:153], v[216:219], v[46:49]
	v_mfma_f32_16x16x32_bf16 v[42:45], v[158:161], v[216:219], v[42:45]
	v_mfma_f32_16x16x32_bf16 v[30:33], v[150:153], v[224:227], v[30:33]
	v_mfma_f32_16x16x32_bf16 v[26:29], v[158:161], v[224:227], v[26:29]
	v_mfma_f32_16x16x32_bf16 v[14:17], v[150:153], v[232:235], v[14:17]
	v_mfma_f32_16x16x32_bf16 v[10:13], v[158:161], v[232:235], v[10:13]
	s_setprio 0
	s_setprio 1
	v_mfma_f32_16x16x32_bf16 v[54:57], v[164:167], v[204:207], v[54:57]
	v_mfma_f32_16x16x32_bf16 v[50:53], v[176:179], v[204:207], v[50:53]
	v_mfma_f32_16x16x32_bf16 v[38:41], v[164:167], v[212:215], v[38:41]
	v_mfma_f32_16x16x32_bf16 v[34:37], v[176:179], v[212:215], v[34:37]
	v_mfma_f32_16x16x32_bf16 v[22:25], v[164:167], v[220:223], v[22:25]
	v_mfma_f32_16x16x32_bf16 v[18:21], v[176:179], v[220:223], v[18:21]
	v_mfma_f32_16x16x32_bf16 v[6:9], v[164:167], v[228:231], v[6:9]
	v_mfma_f32_16x16x32_bf16 v[2:5], v[176:179], v[228:231], v[2:5]
	v_mfma_f32_16x16x32_bf16 v[54:57], v[172:175], v[208:211], v[54:57]
	v_mfma_f32_16x16x32_bf16 v[50:53], v[200:203], v[208:211], v[50:53]
	v_mfma_f32_16x16x32_bf16 v[38:41], v[172:175], v[216:219], v[38:41]
	v_mfma_f32_16x16x32_bf16 v[34:37], v[200:203], v[216:219], v[34:37]
	v_mfma_f32_16x16x32_bf16 v[22:25], v[172:175], v[224:227], v[22:25]
	v_mfma_f32_16x16x32_bf16 v[18:21], v[200:203], v[224:227], v[18:21]
	v_mfma_f32_16x16x32_bf16 v[6:9], v[172:175], v[232:235], v[6:9]
	v_mfma_f32_16x16x32_bf16 v[2:5], v[200:203], v[232:235], v[2:5]
	s_setprio 0
	s_barrier
	s_add_i32 s41, s41, 2
	s_add_u32 s33, s33, 0x100
	s_addc_u32 s40, s40, 0
	s_add_u32 s18, s18, 0x100
	s_addc_u32 s19, s19, 0
	s_cmp_lt_u32 s41, 6
	s_cbranch_scc1 .LBB0_775
	s_andn2_b64 vcc, exec, s[8:9]
	s_cbranch_vccnz .LBB0_778
	s_barrier

.LBB0_843:
	s_add_i32 s33, s26, 0x100
	s_add_u32 s41, s20, s26
	s_addc_u32 s43, s21, 0
	s_add_u32 s42, s41, 0x100
	s_addc_u32 s44, s43, 0
	s_and_b64 s[26:27], s[24:25], exec
	s_cselect_b32 s27, s13, s44
	s_cselect_b32 s26, s19, s42
	s_add_i32 s44, 0, 0x10000
	s_and_b64 s[24:25], s[24:25], exec
	s_cselect_b32 s24, 0, s33
	s_cselect_b32 s25, 0, 0
	s_add_u32 s24, s0, s24
	s_addc_u32 s25, s1, s25
	s_add_i32 s33, 0, 0x14000
	v_add_u32_e32 v134, s44, v172
	v_add_u32_e32 v158, s33, v172
	ds_read_b128 v[102:105], v134
	ds_read_b128 v[114:117], v134 offset:1024
	ds_read_b128 v[126:129], v134 offset:2048
	ds_read_b128 v[134:137], v134 offset:3072
	ds_read_b128 v[138:141], v158
	ds_read_b128 v[146:149], v158 offset:1024
	ds_read_b128 v[154:157], v158 offset:2048
	ds_read_b128 v[158:161], v158 offset:3072
	s_add_u32 s42, s41, 0x10080
	s_addc_u32 s43, s43, 0
	v_lshl_add_u64 v[224:225], s[42:43], 0, v[162:163]
	s_add_i32 m0, s34, 0xc000
	ds_read_b128 v[166:169], v173
	ds_read_b128 v[176:179], v173 offset:1024
	ds_read_b128 v[200:203], v173 offset:2048
	ds_read_b128 v[204:207], v173 offset:3072
	ds_read_b128 v[208:211], v173 offset:4096
	ds_read_b128 v[212:215], v173 offset:5120
	ds_read_b128 v[216:219], v173 offset:6144
	ds_read_b128 v[220:223], v173 offset:7168
	global_load_lds_dwordx4 v[224:225], off
	v_lshl_add_u64 v[224:225], s[42:43], 0, v[164:165]
	s_add_i32 m0, s34, 0xe000
	s_nop 0
	global_load_lds_dwordx4 v[224:225], off
	s_waitcnt vmcnt(8)
	s_waitcnt lgkmcnt(0)
	s_setprio 1
	s_barrier
	v_mfma_f32_16x16x32_bf16 v[150:153], v[102:105], v[166:169], v[150:153]
	v_mfma_f32_16x16x32_bf16 v[142:145], v[126:129], v[166:169], v[142:145]
	v_mfma_f32_16x16x32_bf16 v[118:121], v[102:105], v[200:203], v[118:121]
	v_mfma_f32_16x16x32_bf16 v[110:113], v[126:129], v[200:203], v[110:113]
	v_mfma_f32_16x16x32_bf16 v[94:97], v[102:105], v[208:211], v[94:97]
	v_mfma_f32_16x16x32_bf16 v[90:93], v[126:129], v[208:211], v[90:93]
	v_mfma_f32_16x16x32_bf16 v[78:81], v[102:105], v[216:219], v[78:81]
	v_mfma_f32_16x16x32_bf16 v[74:77], v[126:129], v[216:219], v[74:77]
	v_mfma_f32_16x16x32_bf16 v[150:153], v[114:117], v[176:179], v[150:153]
	v_mfma_f32_16x16x32_bf16 v[142:145], v[134:137], v[176:179], v[142:145]
	v_mfma_f32_16x16x32_bf16 v[118:121], v[114:117], v[204:207], v[118:121]
	v_mfma_f32_16x16x32_bf16 v[110:113], v[134:137], v[204:207], v[110:113]
	v_mfma_f32_16x16x32_bf16 v[94:97], v[114:117], v[212:215], v[94:97]
	v_mfma_f32_16x16x32_bf16 v[90:93], v[134:137], v[212:215], v[90:93]
	v_mfma_f32_16x16x32_bf16 v[78:81], v[114:117], v[220:223], v[78:81]
	v_mfma_f32_16x16x32_bf16 v[74:77], v[134:137], v[220:223], v[74:77]
	s_setprio 0
	s_setprio 1
	v_mfma_f32_16x16x32_bf16 v[130:133], v[138:141], v[166:169], v[130:133]
	v_mfma_f32_16x16x32_bf16 v[122:125], v[154:157], v[166:169], v[122:125]
	v_mfma_f32_16x16x32_bf16 v[106:109], v[138:141], v[200:203], v[106:109]
	v_mfma_f32_16x16x32_bf16 v[98:101], v[154:157], v[200:203], v[98:101]
	v_mfma_f32_16x16x32_bf16 v[86:89], v[138:141], v[208:211], v[86:89]
	v_mfma_f32_16x16x32_bf16 v[82:85], v[154:157], v[208:211], v[82:85]
	v_mfma_f32_16x16x32_bf16 v[70:73], v[138:141], v[216:219], v[70:73]
	v_mfma_f32_16x16x32_bf16 v[66:69], v[154:157], v[216:219], v[66:69]
	v_mfma_f32_16x16x32_bf16 v[130:133], v[146:149], v[176:179], v[130:133]
	v_mfma_f32_16x16x32_bf16 v[122:125], v[158:161], v[176:179], v[122:125]
	v_mfma_f32_16x16x32_bf16 v[106:109], v[146:149], v[204:207], v[106:109]
	v_mfma_f32_16x16x32_bf16 v[98:101], v[158:161], v[204:207], v[98:101]
	v_mfma_f32_16x16x32_bf16 v[86:89], v[146:149], v[212:215], v[86:89]
	v_mfma_f32_16x16x32_bf16 v[82:85], v[158:161], v[212:215], v[82:85]
	v_mfma_f32_16x16x32_bf16 v[70:73], v[146:149], v[220:223], v[70:73]
	v_mfma_f32_16x16x32_bf16 v[66:69], v[158:161], v[220:223], v[66:69]
	s_setprio 0
	s_barrier
	s_add_i32 s41, s44, s31
	v_lshl_add_u64 v[224:225], s[24:25], 0, v[162:163]
	s_mov_b32 m0, s41
	ds_read_b128 v[166:169], v173 offset:16384
	ds_read_b128 v[176:179], v173 offset:17408
	ds_read_b128 v[200:203], v173 offset:18432
	ds_read_b128 v[204:207], v173 offset:19456
	ds_read_b128 v[208:211], v173 offset:20480
	ds_read_b128 v[212:215], v173 offset:21504
	ds_read_b128 v[216:219], v173 offset:22528
	ds_read_b128 v[220:223], v173 offset:23552
	global_load_lds_dwordx4 v[224:225], off
	s_add_i32 m0, s41, 0x2000
	s_add_u32 s42, s24, 0x10000
	v_lshl_add_u64 v[226:227], s[24:25], 0, v[164:165]
	s_addc_u32 s43, s25, 0
	s_add_i32 s33, s33, s31
	global_load_lds_dwordx4 v[226:227], off
	v_lshl_add_u64 v[228:229], s[42:43], 0, v[162:163]
	s_mov_b32 m0, s33
	v_lshl_add_u64 v[230:231], s[26:27], 0, v[164:165]
	global_load_lds_dwordx4 v[228:229], off
	v_lshl_add_u64 v[228:229], s[42:43], 0, v[164:165]
	s_add_i32 m0, s33, 0x2000
	s_nop 0
	global_load_lds_dwordx4 v[228:229], off
	v_lshl_add_u64 v[228:229], s[26:27], 0, v[162:163]
	s_mov_b32 m0, s34
	s_nop 0
	global_load_lds_dwordx4 v[228:229], off
	s_mov_b32 m0, s35
	s_nop 0
	global_load_lds_dwordx4 v[230:231], off
	s_waitcnt vmcnt(8)
	s_waitcnt lgkmcnt(0)
	s_setprio 1
	s_barrier
	v_mfma_f32_16x16x32_bf16 v[62:65], v[102:105], v[166:169], v[62:65]
	v_mfma_f32_16x16x32_bf16 v[58:61], v[126:129], v[166:169], v[58:61]
	v_mfma_f32_16x16x32_bf16 v[46:49], v[102:105], v[200:203], v[46:49]
	v_mfma_f32_16x16x32_bf16 v[42:45], v[126:129], v[200:203], v[42:45]
	v_mfma_f32_16x16x32_bf16 v[30:33], v[102:105], v[208:211], v[30:33]
	v_mfma_f32_16x16x32_bf16 v[26:29], v[126:129], v[208:211], v[26:29]
	v_mfma_f32_16x16x32_bf16 v[14:17], v[102:105], v[216:219], v[14:17]
	v_mfma_f32_16x16x32_bf16 v[10:13], v[126:129], v[216:219], v[10:13]
	v_mfma_f32_16x16x32_bf16 v[62:65], v[114:117], v[176:179], v[62:65]
	v_mfma_f32_16x16x32_bf16 v[58:61], v[134:137], v[176:179], v[58:61]
	v_mfma_f32_16x16x32_bf16 v[46:49], v[114:117], v[204:207], v[46:49]
	v_mfma_f32_16x16x32_bf16 v[42:45], v[134:137], v[204:207], v[42:45]
	v_mfma_f32_16x16x32_bf16 v[30:33], v[114:117], v[212:215], v[30:33]
	v_mfma_f32_16x16x32_bf16 v[26:29], v[134:137], v[212:215], v[26:29]
	v_mfma_f32_16x16x32_bf16 v[14:17], v[114:117], v[220:223], v[14:17]
	v_mfma_f32_16x16x32_bf16 v[10:13], v[134:137], v[220:223], v[10:13]
	s_setprio 0
	s_setprio 1
	v_mfma_f32_16x16x32_bf16 v[54:57], v[138:141], v[166:169], v[54:57]
	v_mfma_f32_16x16x32_bf16 v[50:53], v[154:157], v[166:169], v[50:53]
	v_mfma_f32_16x16x32_bf16 v[38:41], v[138:141], v[200:203], v[38:41]
	v_mfma_f32_16x16x32_bf16 v[34:37], v[154:157], v[200:203], v[34:37]
	v_mfma_f32_16x16x32_bf16 v[22:25], v[138:141], v[208:211], v[22:25]
	v_mfma_f32_16x16x32_bf16 v[18:21], v[154:157], v[208:211], v[18:21]
	v_mfma_f32_16x16x32_bf16 v[6:9], v[138:141], v[216:219], v[6:9]
	v_mfma_f32_16x16x32_bf16 v[2:5], v[154:157], v[216:219], v[2:5]
	v_mfma_f32_16x16x32_bf16 v[54:57], v[146:149], v[176:179], v[54:57]
	v_mfma_f32_16x16x32_bf16 v[50:53], v[158:161], v[176:179], v[50:53]
	v_mfma_f32_16x16x32_bf16 v[38:41], v[146:149], v[204:207], v[38:41]
	v_mfma_f32_16x16x32_bf16 v[34:37], v[158:161], v[204:207], v[34:37]
	v_mfma_f32_16x16x32_bf16 v[22:25], v[146:149], v[212:215], v[22:25]
	v_mfma_f32_16x16x32_bf16 v[18:21], v[158:161], v[212:215], v[18:21]
	v_mfma_f32_16x16x32_bf16 v[6:9], v[146:149], v[220:223], v[6:9]
	v_mfma_f32_16x16x32_bf16 v[2:5], v[158:161], v[220:223], v[2:5]
	s_setprio 0
	s_barrier
	s_add_i32 s33, 0, 0x18000
	s_add_i32 s41, 0, 0x1c000
	v_add_u32_e32 v134, s33, v172
	v_add_u32_e32 v158, s41, v172
	ds_read_b128 v[102:105], v134
	ds_read_b128 v[114:117], v134 offset:1024
	ds_read_b128 v[126:129], v134 offset:2048
	ds_read_b128 v[134:137], v134 offset:3072
	ds_read_b128 v[138:141], v158
	ds_read_b128 v[146:149], v158 offset:1024
	ds_read_b128 v[154:157], v158 offset:2048
	ds_read_b128 v[158:161], v158 offset:3072
	s_add_u32 s26, s26, 0x10000
	s_addc_u32 s27, s27, 0
	s_mov_b32 m0, s36
	v_lshl_add_u64 v[232:233], s[26:27], 0, v[162:163]
	ds_read_b128 v[166:169], v173 offset:32768
	ds_read_b128 v[176:179], v173 offset:33792
	ds_read_b128 v[200:203], v173 offset:34816
	ds_read_b128 v[204:207], v173 offset:35840
	ds_read_b128 v[208:211], v173 offset:36864
	ds_read_b128 v[212:215], v173 offset:37888
	ds_read_b128 v[216:219], v173 offset:38912
	ds_read_b128 v[220:223], v173 offset:39936
	global_load_lds_dwordx4 v[232:233], off
	v_lshl_add_u64 v[232:233], s[26:27], 0, v[164:165]
	s_mov_b32 m0, s37
	s_nop 0
	global_load_lds_dwordx4 v[232:233], off
	s_waitcnt vmcnt(8)
	s_waitcnt lgkmcnt(0)
	s_setprio 1
	s_barrier
	v_mfma_f32_16x16x32_bf16 v[150:153], v[102:105], v[166:169], v[150:153]
	v_mfma_f32_16x16x32_bf16 v[142:145], v[126:129], v[166:169], v[142:145]
	v_mfma_f32_16x16x32_bf16 v[118:121], v[102:105], v[200:203], v[118:121]
	v_mfma_f32_16x16x32_bf16 v[110:113], v[126:129], v[200:203], v[110:113]
	v_mfma_f32_16x16x32_bf16 v[94:97], v[102:105], v[208:211], v[94:97]
	v_mfma_f32_16x16x32_bf16 v[90:93], v[126:129], v[208:211], v[90:93]
	v_mfma_f32_16x16x32_bf16 v[78:81], v[102:105], v[216:219], v[78:81]
	v_mfma_f32_16x16x32_bf16 v[74:77], v[126:129], v[216:219], v[74:77]
	v_mfma_f32_16x16x32_bf16 v[150:153], v[114:117], v[176:179], v[150:153]
	v_mfma_f32_16x16x32_bf16 v[142:145], v[134:137], v[176:179], v[142:145]
	v_mfma_f32_16x16x32_bf16 v[118:121], v[114:117], v[204:207], v[118:121]
	v_mfma_f32_16x16x32_bf16 v[110:113], v[134:137], v[204:207], v[110:113]
	v_mfma_f32_16x16x32_bf16 v[94:97], v[114:117], v[212:215], v[94:97]
	v_mfma_f32_16x16x32_bf16 v[90:93], v[134:137], v[212:215], v[90:93]
	v_mfma_f32_16x16x32_bf16 v[78:81], v[114:117], v[220:223], v[78:81]
	v_mfma_f32_16x16x32_bf16 v[74:77], v[134:137], v[220:223], v[74:77]
	s_setprio 0
	s_setprio 1
	v_mfma_f32_16x16x32_bf16 v[130:133], v[138:141], v[166:169], v[130:133]
	v_mfma_f32_16x16x32_bf16 v[122:125], v[154:157], v[166:169], v[122:125]
	v_mfma_f32_16x16x32_bf16 v[106:109], v[138:141], v[200:203], v[106:109]
	v_mfma_f32_16x16x32_bf16 v[98:101], v[154:157], v[200:203], v[98:101]
	v_mfma_f32_16x16x32_bf16 v[86:89], v[138:141], v[208:211], v[86:89]
	v_mfma_f32_16x16x32_bf16 v[82:85], v[154:157], v[208:211], v[82:85]
	v_mfma_f32_16x16x32_bf16 v[70:73], v[138:141], v[216:219], v[70:73]
	v_mfma_f32_16x16x32_bf16 v[66:69], v[154:157], v[216:219], v[66:69]
	v_mfma_f32_16x16x32_bf16 v[130:133], v[146:149], v[176:179], v[130:133]
	v_mfma_f32_16x16x32_bf16 v[122:125], v[158:161], v[176:179], v[122:125]
	v_mfma_f32_16x16x32_bf16 v[106:109], v[146:149], v[204:207], v[106:109]
	v_mfma_f32_16x16x32_bf16 v[98:101], v[158:161], v[204:207], v[98:101]
	v_mfma_f32_16x16x32_bf16 v[86:89], v[146:149], v[212:215], v[86:89]
	v_mfma_f32_16x16x32_bf16 v[82:85], v[158:161], v[212:215], v[82:85]
	v_mfma_f32_16x16x32_bf16 v[70:73], v[146:149], v[220:223], v[70:73]
	v_mfma_f32_16x16x32_bf16 v[66:69], v[158:161], v[220:223], v[66:69]
	s_setprio 0
	s_barrier
	s_add_i32 s26, s33, s31
	v_lshl_add_u64 v[224:225], v[224:225], 0, s[90:91]
	s_mov_b32 m0, s26
	ds_read_b128 v[166:169], v173 offset:49152
	ds_read_b128 v[176:179], v173 offset:50176
	ds_read_b128 v[200:203], v173 offset:51200
	ds_read_b128 v[204:207], v173 offset:52224
	ds_read_b128 v[208:211], v173 offset:53248
	ds_read_b128 v[212:215], v173 offset:54272
	ds_read_b128 v[216:219], v173 offset:55296
	ds_read_b128 v[220:223], v173 offset:56320
	global_load_lds_dwordx4 v[224:225], off
	s_add_i32 m0, s26, 0x2000
	s_add_u32 s24, s24, 0x10080
	v_lshl_add_u64 v[224:225], v[226:227], 0, s[90:91]
	s_addc_u32 s25, s25, 0
	s_add_i32 s26, s41, s31
	global_load_lds_dwordx4 v[224:225], off
	v_lshl_add_u64 v[224:225], s[24:25], 0, v[162:163]
	s_mov_b32 m0, s26
	s_nop 0
	global_load_lds_dwordx4 v[224:225], off
	v_lshl_add_u64 v[224:225], s[24:25], 0, v[164:165]
	s_add_i32 m0, s26, 0x2000
	s_nop 0
	global_load_lds_dwordx4 v[224:225], off
	v_lshl_add_u64 v[224:225], v[228:229], 0, s[90:91]
	s_mov_b32 m0, s38
	s_nop 0
	global_load_lds_dwordx4 v[224:225], off
	v_lshl_add_u64 v[224:225], v[230:231], 0, s[90:91]
	s_mov_b32 m0, s39
	s_nop 0
	global_load_lds_dwordx4 v[224:225], off
	s_waitcnt vmcnt(8)
	s_waitcnt lgkmcnt(0)
	s_setprio 1
	s_barrier
	v_mfma_f32_16x16x32_bf16 v[62:65], v[102:105], v[166:169], v[62:65]
	v_mfma_f32_16x16x32_bf16 v[58:61], v[126:129], v[166:169], v[58:61]
	v_mfma_f32_16x16x32_bf16 v[46:49], v[102:105], v[200:203], v[46:49]
	v_mfma_f32_16x16x32_bf16 v[42:45], v[126:129], v[200:203], v[42:45]
	v_mfma_f32_16x16x32_bf16 v[30:33], v[102:105], v[208:211], v[30:33]
	v_mfma_f32_16x16x32_bf16 v[26:29], v[126:129], v[208:211], v[26:29]
	v_mfma_f32_16x16x32_bf16 v[14:17], v[102:105], v[216:219], v[14:17]
	v_mfma_f32_16x16x32_bf16 v[10:13], v[126:129], v[216:219], v[10:13]
	v_mfma_f32_16x16x32_bf16 v[62:65], v[114:117], v[176:179], v[62:65]
	v_mfma_f32_16x16x32_bf16 v[58:61], v[134:137], v[176:179], v[58:61]
	v_mfma_f32_16x16x32_bf16 v[46:49], v[114:117], v[204:207], v[46:49]
	v_mfma_f32_16x16x32_bf16 v[42:45], v[134:137], v[204:207], v[42:45]
	v_mfma_f32_16x16x32_bf16 v[30:33], v[114:117], v[212:215], v[30:33]
	v_mfma_f32_16x16x32_bf16 v[26:29], v[134:137], v[212:215], v[26:29]
	v_mfma_f32_16x16x32_bf16 v[14:17], v[114:117], v[220:223], v[14:17]
	v_mfma_f32_16x16x32_bf16 v[10:13], v[134:137], v[220:223], v[10:13]
	s_setprio 0
	s_setprio 1
	v_mfma_f32_16x16x32_bf16 v[54:57], v[138:141], v[166:169], v[54:57]
	v_mfma_f32_16x16x32_bf16 v[50:53], v[154:157], v[166:169], v[50:53]
	v_mfma_f32_16x16x32_bf16 v[38:41], v[138:141], v[200:203], v[38:41]
	v_mfma_f32_16x16x32_bf16 v[34:37], v[154:157], v[200:203], v[34:37]
	v_mfma_f32_16x16x32_bf16 v[22:25], v[138:141], v[208:211], v[22:25]
	v_mfma_f32_16x16x32_bf16 v[18:21], v[154:157], v[208:211], v[18:21]
	v_mfma_f32_16x16x32_bf16 v[6:9], v[138:141], v[216:219], v[6:9]
	v_mfma_f32_16x16x32_bf16 v[2:5], v[154:157], v[216:219], v[2:5]
	v_mfma_f32_16x16x32_bf16 v[54:57], v[146:149], v[176:179], v[54:57]
	v_mfma_f32_16x16x32_bf16 v[50:53], v[158:161], v[176:179], v[50:53]
	v_mfma_f32_16x16x32_bf16 v[38:41], v[146:149], v[204:207], v[38:41]
	v_mfma_f32_16x16x32_bf16 v[34:37], v[158:161], v[204:207], v[34:37]
	v_mfma_f32_16x16x32_bf16 v[22:25], v[146:149], v[212:215], v[22:25]
	v_mfma_f32_16x16x32_bf16 v[18:21], v[158:161], v[212:215], v[18:21]
	v_mfma_f32_16x16x32_bf16 v[6:9], v[146:149], v[220:223], v[6:9]
	v_mfma_f32_16x16x32_bf16 v[2:5], v[158:161], v[220:223], v[2:5]
	s_setprio 0
	s_barrier
	s_and_b64 vcc, exec, s[22:23]
	s_mov_b64 s[24:25], -1
	s_mov_b64 s[22:23], 0
	s_movk_i32 s26, 0x100
	s_cbranch_vccnz .LBB0_843
	s_andn2_b64 vcc, exec, s[10:11]
	s_cbranch_vccnz .LBB0_846
	s_barrier

.LBB0_996:
	s_add_u32 s22, s20, 0xfffc0080
	s_addc_u32 s23, s21, -1
	s_add_i32 s45, 0, 0x10000
	s_cmp_eq_u32 s44, 12
	s_cselect_b32 s25, s9, s23
	s_cselect_b32 s24, s40, s22
	s_cselect_b32 s23, s11, s43
	s_cselect_b32 s22, s41, s42
	s_add_i32 s48, 0, 0x14000
	v_add_u32_e32 v142, s45, v171
	v_add_u32_e32 v168, s48, v171
	ds_read_b128 v[130:133], v142
	ds_read_b128 v[134:137], v142 offset:1024
	ds_read_b128 v[138:141], v142 offset:2048
	ds_read_b128 v[142:145], v142 offset:3072
	ds_read_b128 v[146:149], v168
	ds_read_b128 v[158:161], v168 offset:1024
	ds_read_b128 v[164:167], v168 offset:2048
	ds_read_b128 v[174:177], v168 offset:3072
	v_lshl_add_u64 v[168:169], s[20:21], 0, v[156:157]
	s_add_i32 m0, s33, 0xc000
	ds_read_b128 v[200:203], v172
	ds_read_b128 v[204:207], v172 offset:1024
	ds_read_b128 v[208:211], v172 offset:2048
	ds_read_b128 v[212:215], v172 offset:3072
	ds_read_b128 v[216:219], v172 offset:4096
	ds_read_b128 v[220:223], v172 offset:5120
	ds_read_b128 v[224:227], v172 offset:6144
	ds_read_b128 v[228:231], v172 offset:7168
	global_load_lds_dwordx4 v[168:169], off
	v_lshl_add_u64 v[168:169], s[20:21], 0, v[154:155]
	s_add_i32 m0, s33, 0xe000
	s_nop 0
	global_load_lds_dwordx4 v[168:169], off
	s_waitcnt vmcnt(8)
	s_waitcnt lgkmcnt(0)
	s_setprio 1
	s_barrier
	v_mfma_f32_16x16x32_bf16 v[126:129], v[130:133], v[200:203], v[126:129]
	v_mfma_f32_16x16x32_bf16 v[122:125], v[138:141], v[200:203], v[122:125]
	v_mfma_f32_16x16x32_bf16 v[110:113], v[130:133], v[208:211], v[110:113]
	v_mfma_f32_16x16x32_bf16 v[106:109], v[138:141], v[208:211], v[106:109]
	v_mfma_f32_16x16x32_bf16 v[98:101], v[130:133], v[216:219], v[98:101]
	v_mfma_f32_16x16x32_bf16 v[90:93], v[138:141], v[216:219], v[90:93]
	v_mfma_f32_16x16x32_bf16 v[86:89], v[130:133], v[224:227], v[86:89]
	v_mfma_f32_16x16x32_bf16 v[78:81], v[138:141], v[224:227], v[78:81]
	v_mfma_f32_16x16x32_bf16 v[126:129], v[134:137], v[204:207], v[126:129]
	v_mfma_f32_16x16x32_bf16 v[122:125], v[142:145], v[204:207], v[122:125]
	v_mfma_f32_16x16x32_bf16 v[110:113], v[134:137], v[212:215], v[110:113]
	v_mfma_f32_16x16x32_bf16 v[106:109], v[142:145], v[212:215], v[106:109]
	v_mfma_f32_16x16x32_bf16 v[98:101], v[134:137], v[220:223], v[98:101]
	v_mfma_f32_16x16x32_bf16 v[90:93], v[142:145], v[220:223], v[90:93]
	v_mfma_f32_16x16x32_bf16 v[86:89], v[134:137], v[228:231], v[86:89]
	v_mfma_f32_16x16x32_bf16 v[78:81], v[142:145], v[228:231], v[78:81]
	s_setprio 0
	s_setprio 1
	v_mfma_f32_16x16x32_bf16 v[118:121], v[146:149], v[200:203], v[118:121]
	v_mfma_f32_16x16x32_bf16 v[114:117], v[164:167], v[200:203], v[114:117]
	v_mfma_f32_16x16x32_bf16 v[102:105], v[146:149], v[208:211], v[102:105]
	v_mfma_f32_16x16x32_bf16 v[94:97], v[164:167], v[208:211], v[94:97]
	v_mfma_f32_16x16x32_bf16 v[82:85], v[146:149], v[216:219], v[82:85]
	v_mfma_f32_16x16x32_bf16 v[74:77], v[164:167], v[216:219], v[74:77]
	v_mfma_f32_16x16x32_bf16 v[70:73], v[146:149], v[224:227], v[70:73]
	v_mfma_f32_16x16x32_bf16 v[66:69], v[164:167], v[224:227], v[66:69]
	v_mfma_f32_16x16x32_bf16 v[118:121], v[158:161], v[204:207], v[118:121]
	v_mfma_f32_16x16x32_bf16 v[114:117], v[174:177], v[204:207], v[114:117]
	v_mfma_f32_16x16x32_bf16 v[102:105], v[158:161], v[212:215], v[102:105]
	v_mfma_f32_16x16x32_bf16 v[94:97], v[174:177], v[212:215], v[94:97]
	v_mfma_f32_16x16x32_bf16 v[82:85], v[158:161], v[220:223], v[82:85]
	v_mfma_f32_16x16x32_bf16 v[74:77], v[174:177], v[220:223], v[74:77]
	v_mfma_f32_16x16x32_bf16 v[70:73], v[158:161], v[228:231], v[70:73]
	v_mfma_f32_16x16x32_bf16 v[66:69], v[174:177], v[228:231], v[66:69]
	s_setprio 0
	s_barrier
	s_add_i32 s45, s45, s31
	v_lshl_add_u64 v[168:169], s[22:23], 0, v[162:163]
	s_mov_b32 m0, s45
	ds_read_b128 v[200:203], v172 offset:16384
	ds_read_b128 v[204:207], v172 offset:17408
	ds_read_b128 v[208:211], v172 offset:18432
	ds_read_b128 v[212:215], v172 offset:19456
	ds_read_b128 v[216:219], v172 offset:20480
	ds_read_b128 v[220:223], v172 offset:21504
	ds_read_b128 v[224:227], v172 offset:22528
	ds_read_b128 v[228:231], v172 offset:23552
	global_load_lds_dwordx4 v[168:169], off
	s_add_i32 m0, s45, 0x2000
	s_add_u32 s46, s22, 0x40000
	v_lshl_add_u64 v[178:179], s[22:23], 0, v[150:151]
	s_addc_u32 s47, s23, 0
	s_add_i32 s45, s48, s31
	global_load_lds_dwordx4 v[178:179], off
	v_lshl_add_u64 v[232:233], s[46:47], 0, v[162:163]
	s_mov_b32 m0, s45
	v_lshl_add_u64 v[234:235], s[24:25], 0, v[150:151]
	global_load_lds_dwordx4 v[232:233], off
	v_lshl_add_u64 v[232:233], s[46:47], 0, v[150:151]
	s_add_i32 m0, s45, 0x2000
	s_nop 0
	global_load_lds_dwordx4 v[232:233], off
	v_lshl_add_u64 v[232:233], s[24:25], 0, v[162:163]
	s_mov_b32 m0, s33
	s_nop 0
	global_load_lds_dwordx4 v[232:233], off
	s_mov_b32 m0, s34
	s_nop 0
	global_load_lds_dwordx4 v[234:235], off
	s_waitcnt vmcnt(8)
	s_waitcnt lgkmcnt(0)
	s_setprio 1
	s_barrier
	v_mfma_f32_16x16x32_bf16 v[62:65], v[130:133], v[200:203], v[62:65]
	v_mfma_f32_16x16x32_bf16 v[58:61], v[138:141], v[200:203], v[58:61]
	v_mfma_f32_16x16x32_bf16 v[50:53], v[130:133], v[208:211], v[50:53]
	v_mfma_f32_16x16x32_bf16 v[42:45], v[138:141], v[208:211], v[42:45]
	v_mfma_f32_16x16x32_bf16 v[34:37], v[130:133], v[216:219], v[34:37]
	v_mfma_f32_16x16x32_bf16 v[26:29], v[138:141], v[216:219], v[26:29]
	v_mfma_f32_16x16x32_bf16 v[18:21], v[130:133], v[224:227], v[18:21]
	v_mfma_f32_16x16x32_bf16 v[10:13], v[138:141], v[224:227], v[10:13]
	v_mfma_f32_16x16x32_bf16 v[62:65], v[134:137], v[204:207], v[62:65]
	v_mfma_f32_16x16x32_bf16 v[58:61], v[142:145], v[204:207], v[58:61]
	v_mfma_f32_16x16x32_bf16 v[50:53], v[134:137], v[212:215], v[50:53]
	v_mfma_f32_16x16x32_bf16 v[42:45], v[142:145], v[212:215], v[42:45]
	v_mfma_f32_16x16x32_bf16 v[34:37], v[134:137], v[220:223], v[34:37]
	v_mfma_f32_16x16x32_bf16 v[26:29], v[142:145], v[220:223], v[26:29]
	v_mfma_f32_16x16x32_bf16 v[18:21], v[134:137], v[228:231], v[18:21]
	v_mfma_f32_16x16x32_bf16 v[10:13], v[142:145], v[228:231], v[10:13]
	s_setprio 0
	s_setprio 1
	v_mfma_f32_16x16x32_bf16 v[54:57], v[146:149], v[200:203], v[54:57]
	v_mfma_f32_16x16x32_bf16 v[46:49], v[164:167], v[200:203], v[46:49]
	v_mfma_f32_16x16x32_bf16 v[38:41], v[146:149], v[208:211], v[38:41]
	v_mfma_f32_16x16x32_bf16 v[30:33], v[164:167], v[208:211], v[30:33]
	v_mfma_f32_16x16x32_bf16 v[22:25], v[146:149], v[216:219], v[22:25]
	v_mfma_f32_16x16x32_bf16 v[14:17], v[164:167], v[216:219], v[14:17]
	v_mfma_f32_16x16x32_bf16 v[6:9], v[146:149], v[224:227], v[6:9]
	v_mfma_f32_16x16x32_bf16 v[2:5], v[164:167], v[224:227], v[2:5]
	v_mfma_f32_16x16x32_bf16 v[54:57], v[158:161], v[204:207], v[54:57]
	v_mfma_f32_16x16x32_bf16 v[46:49], v[174:177], v[204:207], v[46:49]
	v_mfma_f32_16x16x32_bf16 v[38:41], v[158:161], v[212:215], v[38:41]
	v_mfma_f32_16x16x32_bf16 v[30:33], v[174:177], v[212:215], v[30:33]
	v_mfma_f32_16x16x32_bf16 v[22:25], v[158:161], v[220:223], v[22:25]
	v_mfma_f32_16x16x32_bf16 v[14:17], v[174:177], v[220:223], v[14:17]
	v_mfma_f32_16x16x32_bf16 v[6:9], v[158:161], v[228:231], v[6:9]
	v_mfma_f32_16x16x32_bf16 v[2:5], v[174:177], v[228:231], v[2:5]
	s_setprio 0
	s_barrier
	s_add_i32 s45, 0, 0x18000
	s_add_i32 s46, 0, 0x1c000
	v_add_u32_e32 v142, s45, v171
	v_add_u32_e32 v173, s46, v171
	ds_read_b128 v[130:133], v142
	ds_read_b128 v[134:137], v142 offset:1024
	ds_read_b128 v[138:141], v142 offset:2048
	ds_read_b128 v[142:145], v142 offset:3072
	ds_read_b128 v[146:149], v173
	ds_read_b128 v[158:161], v173 offset:1024
	ds_read_b128 v[164:167], v173 offset:2048
	ds_read_b128 v[174:177], v173 offset:3072
	s_add_u32 s24, s24, 0x40000
	s_addc_u32 s25, s25, 0
	s_mov_b32 m0, s35
	v_lshl_add_u64 v[236:237], s[24:25], 0, v[162:163]
	ds_read_b128 v[200:203], v172 offset:32768
	ds_read_b128 v[204:207], v172 offset:33792
	ds_read_b128 v[208:211], v172 offset:34816
	ds_read_b128 v[212:215], v172 offset:35840
	ds_read_b128 v[216:219], v172 offset:36864
	ds_read_b128 v[220:223], v172 offset:37888
	ds_read_b128 v[224:227], v172 offset:38912
	ds_read_b128 v[228:231], v172 offset:39936
	global_load_lds_dwordx4 v[236:237], off
	v_lshl_add_u64 v[236:237], s[24:25], 0, v[150:151]
	s_mov_b32 m0, s36
	s_nop 0
	global_load_lds_dwordx4 v[236:237], off
	s_waitcnt vmcnt(8)
	s_waitcnt lgkmcnt(0)
	s_setprio 1
	s_barrier
	v_mfma_f32_16x16x32_bf16 v[126:129], v[130:133], v[200:203], v[126:129]
	v_mfma_f32_16x16x32_bf16 v[122:125], v[138:141], v[200:203], v[122:125]
	v_mfma_f32_16x16x32_bf16 v[110:113], v[130:133], v[208:211], v[110:113]
	v_mfma_f32_16x16x32_bf16 v[106:109], v[138:141], v[208:211], v[106:109]
	v_mfma_f32_16x16x32_bf16 v[98:101], v[130:133], v[216:219], v[98:101]
	v_mfma_f32_16x16x32_bf16 v[90:93], v[138:141], v[216:219], v[90:93]
	v_mfma_f32_16x16x32_bf16 v[86:89], v[130:133], v[224:227], v[86:89]
	v_mfma_f32_16x16x32_bf16 v[78:81], v[138:141], v[224:227], v[78:81]
	v_mfma_f32_16x16x32_bf16 v[126:129], v[134:137], v[204:207], v[126:129]
	v_mfma_f32_16x16x32_bf16 v[122:125], v[142:145], v[204:207], v[122:125]
	v_mfma_f32_16x16x32_bf16 v[110:113], v[134:137], v[212:215], v[110:113]
	v_mfma_f32_16x16x32_bf16 v[106:109], v[142:145], v[212:215], v[106:109]
	v_mfma_f32_16x16x32_bf16 v[98:101], v[134:137], v[220:223], v[98:101]
	v_mfma_f32_16x16x32_bf16 v[90:93], v[142:145], v[220:223], v[90:93]
	v_mfma_f32_16x16x32_bf16 v[86:89], v[134:137], v[228:231], v[86:89]
	v_mfma_f32_16x16x32_bf16 v[78:81], v[142:145], v[228:231], v[78:81]
	s_setprio 0
	s_setprio 1
	v_mfma_f32_16x16x32_bf16 v[118:121], v[146:149], v[200:203], v[118:121]
	v_mfma_f32_16x16x32_bf16 v[114:117], v[164:167], v[200:203], v[114:117]
	v_mfma_f32_16x16x32_bf16 v[102:105], v[146:149], v[208:211], v[102:105]
	v_mfma_f32_16x16x32_bf16 v[94:97], v[164:167], v[208:211], v[94:97]
	v_mfma_f32_16x16x32_bf16 v[82:85], v[146:149], v[216:219], v[82:85]
	v_mfma_f32_16x16x32_bf16 v[74:77], v[164:167], v[216:219], v[74:77]
	v_mfma_f32_16x16x32_bf16 v[70:73], v[146:149], v[224:227], v[70:73]
	v_mfma_f32_16x16x32_bf16 v[66:69], v[164:167], v[224:227], v[66:69]
	v_mfma_f32_16x16x32_bf16 v[118:121], v[158:161], v[204:207], v[118:121]
	v_mfma_f32_16x16x32_bf16 v[114:117], v[174:177], v[204:207], v[114:117]
	v_mfma_f32_16x16x32_bf16 v[102:105], v[158:161], v[212:215], v[102:105]
	v_mfma_f32_16x16x32_bf16 v[94:97], v[174:177], v[212:215], v[94:97]
	v_mfma_f32_16x16x32_bf16 v[82:85], v[158:161], v[220:223], v[82:85]
	v_mfma_f32_16x16x32_bf16 v[74:77], v[174:177], v[220:223], v[74:77]
	v_mfma_f32_16x16x32_bf16 v[70:73], v[158:161], v[228:231], v[70:73]
	v_mfma_f32_16x16x32_bf16 v[66:69], v[174:177], v[228:231], v[66:69]
	s_setprio 0
	s_barrier
	s_add_i32 s24, s45, s31
	v_lshl_add_u64 v[168:169], v[168:169], 0, s[90:91]
	s_mov_b32 m0, s24
	ds_read_b128 v[200:203], v172 offset:49152
	ds_read_b128 v[204:207], v172 offset:50176
	ds_read_b128 v[208:211], v172 offset:51200
	ds_read_b128 v[212:215], v172 offset:52224
	ds_read_b128 v[216:219], v172 offset:53248
	ds_read_b128 v[220:223], v172 offset:54272
	ds_read_b128 v[224:227], v172 offset:55296
	ds_read_b128 v[228:231], v172 offset:56320
	global_load_lds_dwordx4 v[168:169], off
	s_add_i32 m0, s24, 0x2000
	s_add_u32 s22, s22, 0x40080
	v_lshl_add_u64 v[168:169], v[178:179], 0, s[90:91]
	s_addc_u32 s23, s23, 0
	s_add_i32 s24, s46, s31
	global_load_lds_dwordx4 v[168:169], off
	v_lshl_add_u64 v[168:169], s[22:23], 0, v[162:163]
	s_mov_b32 m0, s24
	s_nop 0
	global_load_lds_dwordx4 v[168:169], off
	v_lshl_add_u64 v[168:169], s[22:23], 0, v[150:151]
	s_add_i32 m0, s24, 0x2000
	s_nop 0
	global_load_lds_dwordx4 v[168:169], off
	v_lshl_add_u64 v[168:169], v[232:233], 0, s[90:91]
	s_mov_b32 m0, s37
	s_nop 0
	global_load_lds_dwordx4 v[168:169], off
	v_lshl_add_u64 v[168:169], v[234:235], 0, s[90:91]
	s_mov_b32 m0, s38
	s_nop 0
	global_load_lds_dwordx4 v[168:169], off
	s_waitcnt vmcnt(8)
	s_waitcnt lgkmcnt(0)
	s_setprio 1
	s_barrier
	v_mfma_f32_16x16x32_bf16 v[62:65], v[130:133], v[200:203], v[62:65]
	v_mfma_f32_16x16x32_bf16 v[58:61], v[138:141], v[200:203], v[58:61]
	v_mfma_f32_16x16x32_bf16 v[50:53], v[130:133], v[208:211], v[50:53]
	v_mfma_f32_16x16x32_bf16 v[42:45], v[138:141], v[208:211], v[42:45]
	v_mfma_f32_16x16x32_bf16 v[34:37], v[130:133], v[216:219], v[34:37]
	v_mfma_f32_16x16x32_bf16 v[26:29], v[138:141], v[216:219], v[26:29]
	v_mfma_f32_16x16x32_bf16 v[18:21], v[130:133], v[224:227], v[18:21]
	v_mfma_f32_16x16x32_bf16 v[10:13], v[138:141], v[224:227], v[10:13]
	v_mfma_f32_16x16x32_bf16 v[62:65], v[134:137], v[204:207], v[62:65]
	v_mfma_f32_16x16x32_bf16 v[58:61], v[142:145], v[204:207], v[58:61]
	v_mfma_f32_16x16x32_bf16 v[50:53], v[134:137], v[212:215], v[50:53]
	v_mfma_f32_16x16x32_bf16 v[42:45], v[142:145], v[212:215], v[42:45]
	v_mfma_f32_16x16x32_bf16 v[34:37], v[134:137], v[220:223], v[34:37]
	v_mfma_f32_16x16x32_bf16 v[26:29], v[142:145], v[220:223], v[26:29]
	v_mfma_f32_16x16x32_bf16 v[18:21], v[134:137], v[228:231], v[18:21]
	v_mfma_f32_16x16x32_bf16 v[10:13], v[142:145], v[228:231], v[10:13]
	s_setprio 0
	s_setprio 1
	v_mfma_f32_16x16x32_bf16 v[54:57], v[146:149], v[200:203], v[54:57]
	v_mfma_f32_16x16x32_bf16 v[46:49], v[164:167], v[200:203], v[46:49]
	v_mfma_f32_16x16x32_bf16 v[38:41], v[146:149], v[208:211], v[38:41]
	v_mfma_f32_16x16x32_bf16 v[30:33], v[164:167], v[208:211], v[30:33]
	v_mfma_f32_16x16x32_bf16 v[22:25], v[146:149], v[216:219], v[22:25]
	v_mfma_f32_16x16x32_bf16 v[14:17], v[164:167], v[216:219], v[14:17]
	v_mfma_f32_16x16x32_bf16 v[6:9], v[146:149], v[224:227], v[6:9]
	v_mfma_f32_16x16x32_bf16 v[2:5], v[164:167], v[224:227], v[2:5]
	v_mfma_f32_16x16x32_bf16 v[54:57], v[158:161], v[204:207], v[54:57]
	v_mfma_f32_16x16x32_bf16 v[46:49], v[174:177], v[204:207], v[46:49]
	v_mfma_f32_16x16x32_bf16 v[38:41], v[158:161], v[212:215], v[38:41]
	v_mfma_f32_16x16x32_bf16 v[30:33], v[174:177], v[212:215], v[30:33]
	v_mfma_f32_16x16x32_bf16 v[22:25], v[158:161], v[220:223], v[22:25]
	v_mfma_f32_16x16x32_bf16 v[14:17], v[174:177], v[220:223], v[14:17]
	v_mfma_f32_16x16x32_bf16 v[6:9], v[158:161], v[228:231], v[6:9]
	v_mfma_f32_16x16x32_bf16 v[2:5], v[174:177], v[228:231], v[2:5]
	s_setprio 0
	s_barrier
	s_add_i32 s44, s44, 2
	s_add_u32 s42, s42, 0x100
	s_addc_u32 s43, s43, 0
	s_add_u32 s20, s20, 0x100
	s_addc_u32 s21, s21, 0
	s_cmp_lt_u32 s44, 14
	s_cbranch_scc1 .LBB0_996
	v_readlane_b32 s40, v254, 24
	s_andn2_b64 vcc, exec, s[6:7]
	v_readlane_b32 s42, v254, 26
	v_readlane_b32 s43, v254, 27
	v_readlane_b32 s44, v254, 28
	v_readlane_b32 s45, v254, 29
	v_readlane_b32 s46, v254, 30
	v_readlane_b32 s47, v254, 31
	v_readlane_b32 s50, v254, 34
	v_readlane_b32 s51, v254, 35
	v_readlane_b32 s41, v254, 25
	v_readlane_b32 s48, v254, 32
	v_readlane_b32 s49, v254, 33
	v_readlane_b32 s52, v254, 36
	v_readlane_b32 s53, v254, 37
	v_readlane_b32 s54, v254, 38
	v_readlane_b32 s55, v254, 39
	s_cbranch_vccnz .LBB0_999
	s_barrier

.LBB0_1303:
	ds_read_b128 v[2:5], v200
	ds_read_b128 v[6:9], v201
	ds_read_b128 v[10:13], v202
	ds_read_b128 v[14:17], v203
	ds_read_b128 v[18:21], v204
	ds_read_b128 v[22:25], v205
	ds_read_b128 v[26:29], v206
	ds_read_b128 v[30:33], v207
	s_lshl_b32 s21, s56, 10
	v_add_u32_e32 v217, s21, v177
	ds_read_b128 v[34:37], v216
	ds_read_b128 v[38:41], v216 offset:1024
	ds_read_b128 v[42:45], v216 offset:2048
	ds_read_b128 v[46:49], v216 offset:3072
	ds_read_b32 v66, v217 offset:512
	ds_read_b128 v[50:53], v216 offset:4096
	ds_read_b128 v[54:57], v216 offset:5120
	ds_read_b128 v[58:61], v216 offset:6144
	ds_read_b128 v[62:65], v216 offset:7168
	s_add_i32 s21, s36, 0xc000
	s_waitcnt lgkmcnt(0)
	v_lshl_add_u32 v66, v66, 10, v176
	s_mov_b32 m0, s21
	s_add_i32 s57, s36, 0xe000
	global_load_lds_dwordx4 v66, s[12:13]
	ds_read_b32 v66, v217 offset:768
	s_mov_b32 m0, s57
	s_waitcnt lgkmcnt(0)
	v_lshl_add_u32 v66, v66, 10, v176
	global_load_lds_dwordx4 v66, s[12:13]
	s_waitcnt vmcnt(8)
	s_waitcnt lgkmcnt(0)
	s_setprio 1
	s_barrier
	v_mfma_f32_16x16x128_f8f6f4 v[154:157], v[2:9], v[34:41], 0
	v_mfma_f32_16x16x128_f8f6f4 v[146:149], v[10:17], v[34:41], 0
	v_mfma_f32_16x16x128_f8f6f4 v[138:141], v[2:9], v[42:49], 0
	v_mfma_f32_16x16x128_f8f6f4 v[130:133], v[10:17], v[42:49], 0
	v_mfma_f32_16x16x128_f8f6f4 v[122:125], v[2:9], v[50:57], 0
	v_mfma_f32_16x16x128_f8f6f4 v[114:117], v[10:17], v[50:57], 0
	v_mfma_f32_16x16x128_f8f6f4 v[106:109], v[2:9], v[58:65], 0
	v_mfma_f32_16x16x128_f8f6f4 v[98:101], v[10:17], v[58:65], 0
	s_setprio 0
	s_setprio 1
	v_mfma_f32_16x16x128_f8f6f4 v[158:161], v[18:25], v[34:41], 0
	v_mfma_f32_16x16x128_f8f6f4 v[150:153], v[26:33], v[34:41], 0
	v_mfma_f32_16x16x128_f8f6f4 v[142:145], v[18:25], v[42:49], 0
	v_mfma_f32_16x16x128_f8f6f4 v[134:137], v[26:33], v[42:49], 0
	v_mfma_f32_16x16x128_f8f6f4 v[126:129], v[18:25], v[50:57], 0
	v_mfma_f32_16x16x128_f8f6f4 v[118:121], v[26:33], v[50:57], 0
	v_mfma_f32_16x16x128_f8f6f4 v[110:113], v[18:25], v[58:65], 0
	v_mfma_f32_16x16x128_f8f6f4 v[102:105], v[26:33], v[58:65], 0
	s_setprio 0
	s_barrier
	v_lshl_add_u64 v[172:173], s[26:27], 0, v[164:165]
	s_mov_b64 s[28:29], 0x100
	s_mov_b32 m0, s37
	v_lshl_add_u64 v[34:35], v[172:173], 0, s[28:29]
	v_lshl_add_u64 v[174:175], s[26:27], 0, v[166:167]
	ds_read_b128 v[218:221], v216 offset:16384
	ds_read_b128 v[222:225], v216 offset:17408
	ds_read_b128 v[226:229], v216 offset:18432
	ds_read_b128 v[230:233], v216 offset:19456
	ds_read_b128 v[234:237], v216 offset:20480
	ds_read_b128 v[238:241], v216 offset:21504
	ds_read_b128 v[242:245], v216 offset:22528
	ds_read_b128 v[246:249], v216 offset:23552
	global_load_lds_dwordx4 v[34:35], off
	v_lshl_add_u64 v[34:35], v[174:175], 0, s[28:29]
	s_add_u32 s28, s26, 0x20100
	s_mov_b32 m0, s38
	s_addc_u32 s29, s27, 0
	global_load_lds_dwordx4 v[34:35], off
	v_lshl_add_u64 v[34:35], s[28:29], 0, v[164:165]
	s_mov_b32 m0, s39
	s_nop 0
	global_load_lds_dwordx4 v[34:35], off
	v_lshl_add_u64 v[34:35], s[28:29], 0, v[166:167]
	s_mov_b32 m0, s40
	s_nop 0
	global_load_lds_dwordx4 v[34:35], off
	ds_read_b32 v34, v217
	s_mov_b32 m0, s36
	s_waitcnt lgkmcnt(0)
	v_lshl_add_u32 v34, v34, 10, v176
	global_load_lds_dwordx4 v34, s[14:15]
	ds_read_b32 v34, v217 offset:256
	s_mov_b32 m0, s41
	s_waitcnt lgkmcnt(0)
	v_lshl_add_u32 v34, v34, 10, v176
	global_load_lds_dwordx4 v34, s[14:15]
	s_waitcnt vmcnt(8)
	s_waitcnt lgkmcnt(0)
	s_setprio 1
	s_barrier
	v_mfma_f32_16x16x128_f8f6f4 v[90:93], v[2:9], v[218:225], 0
	v_mfma_f32_16x16x128_f8f6f4 v[82:85], v[10:17], v[218:225], 0
	v_mfma_f32_16x16x128_f8f6f4 v[74:77], v[2:9], v[226:233], 0
	v_mfma_f32_16x16x128_f8f6f4 v[66:69], v[10:17], v[226:233], 0
	v_mfma_f32_16x16x128_f8f6f4 v[58:61], v[2:9], v[234:241], 0
	v_mfma_f32_16x16x128_f8f6f4 v[50:53], v[10:17], v[234:241], 0
	v_mfma_f32_16x16x128_f8f6f4 v[42:45], v[2:9], v[242:249], 0
	v_mfma_f32_16x16x128_f8f6f4 v[34:37], v[10:17], v[242:249], 0
	s_setprio 0
	s_setprio 1
	v_mfma_f32_16x16x128_f8f6f4 v[94:97], v[18:25], v[218:225], 0
	v_mfma_f32_16x16x128_f8f6f4 v[86:89], v[26:33], v[218:225], 0
	v_mfma_f32_16x16x128_f8f6f4 v[78:81], v[18:25], v[226:233], 0
	v_mfma_f32_16x16x128_f8f6f4 v[70:73], v[26:33], v[226:233], 0
	v_mfma_f32_16x16x128_f8f6f4 v[62:65], v[18:25], v[234:241], 0
	v_mfma_f32_16x16x128_f8f6f4 v[54:57], v[26:33], v[234:241], 0
	v_mfma_f32_16x16x128_f8f6f4 v[46:49], v[18:25], v[242:249], 0
	v_mfma_f32_16x16x128_f8f6f4 v[38:41], v[26:33], v[242:249], 0
	s_setprio 0
	s_barrier
	ds_read_b128 v[18:21], v208
	ds_read_b128 v[22:25], v209
	ds_read_b128 v[26:29], v210
	ds_read_b128 v[30:33], v211
	ds_read_b128 v[2:5], v212
	ds_read_b128 v[6:9], v213
	ds_read_b128 v[10:13], v214
	ds_read_b128 v[14:17], v215
	ds_read_b128 v[218:221], v216 offset:32768
	ds_read_b128 v[222:225], v216 offset:33792
	ds_read_b128 v[226:229], v216 offset:34816
	ds_read_b128 v[230:233], v216 offset:35840
	ds_read_b32 v162, v217 offset:512
	ds_read_b128 v[234:237], v216 offset:36864
	ds_read_b128 v[238:241], v216 offset:37888
	ds_read_b128 v[242:245], v216 offset:38912
	ds_read_b128 v[246:249], v216 offset:39936
	s_waitcnt lgkmcnt(0)
	v_lshl_add_u32 v162, v162, 10, v176
	s_mov_b32 m0, s42
	s_nop 0
	global_load_lds_dwordx4 v162, s[14:15]
	ds_read_b32 v162, v217 offset:768
	s_mov_b32 m0, s43
	s_waitcnt lgkmcnt(0)
	v_lshl_add_u32 v162, v162, 10, v176
	global_load_lds_dwordx4 v162, s[14:15]
	s_waitcnt vmcnt(8)
	s_waitcnt lgkmcnt(0)
	s_setprio 1
	s_barrier
	v_mfma_f32_16x16x128_f8f6f4 v[154:157], v[18:25], v[218:225], v[154:157]
	v_mfma_f32_16x16x128_f8f6f4 v[146:149], v[26:33], v[218:225], v[146:149]
	v_mfma_f32_16x16x128_f8f6f4 v[138:141], v[18:25], v[226:233], v[138:141]
	v_mfma_f32_16x16x128_f8f6f4 v[130:133], v[26:33], v[226:233], v[130:133]
	v_mfma_f32_16x16x128_f8f6f4 v[122:125], v[18:25], v[234:241], v[122:125]
	v_mfma_f32_16x16x128_f8f6f4 v[114:117], v[26:33], v[234:241], v[114:117]
	v_mfma_f32_16x16x128_f8f6f4 v[106:109], v[18:25], v[242:249], v[106:109]
	v_mfma_f32_16x16x128_f8f6f4 v[98:101], v[26:33], v[242:249], v[98:101]
	s_setprio 0
	s_setprio 1
	v_mfma_f32_16x16x128_f8f6f4 v[158:161], v[2:9], v[218:225], v[158:161]
	v_mfma_f32_16x16x128_f8f6f4 v[150:153], v[10:17], v[218:225], v[150:153]
	v_mfma_f32_16x16x128_f8f6f4 v[142:145], v[2:9], v[226:233], v[142:145]
	v_mfma_f32_16x16x128_f8f6f4 v[134:137], v[10:17], v[226:233], v[134:137]
	v_mfma_f32_16x16x128_f8f6f4 v[126:129], v[2:9], v[234:241], v[126:129]
	v_mfma_f32_16x16x128_f8f6f4 v[118:121], v[10:17], v[234:241], v[118:121]
	v_mfma_f32_16x16x128_f8f6f4 v[110:113], v[2:9], v[242:249], v[110:113]
	v_mfma_f32_16x16x128_f8f6f4 v[102:105], v[10:17], v[242:249], v[102:105]
	s_setprio 0
	s_barrier
	s_mov_b64 s[28:29], 0x180
	s_mov_b32 m0, s44
	v_lshl_add_u64 v[172:173], v[172:173], 0, s[28:29]
	ds_read_b128 v[218:221], v216 offset:49152
	ds_read_b128 v[222:225], v216 offset:50176
	ds_read_b128 v[226:229], v216 offset:51200
	ds_read_b128 v[230:233], v216 offset:52224
	ds_read_b128 v[234:237], v216 offset:53248
	ds_read_b128 v[238:241], v216 offset:54272
	ds_read_b128 v[242:245], v216 offset:55296
	ds_read_b128 v[246:249], v216 offset:56320
	global_load_lds_dwordx4 v[172:173], off
	v_lshl_add_u64 v[172:173], v[174:175], 0, s[28:29]
	s_add_u32 s28, s26, 0x20180
	s_mov_b32 m0, s45
	s_addc_u32 s29, s27, 0
	global_load_lds_dwordx4 v[172:173], off
	v_lshl_add_u64 v[172:173], s[28:29], 0, v[164:165]
	s_mov_b32 m0, s48
	s_nop 0
	global_load_lds_dwordx4 v[172:173], off
	v_lshl_add_u64 v[172:173], s[28:29], 0, v[166:167]
	s_mov_b32 m0, s49
	s_nop 0
	global_load_lds_dwordx4 v[172:173], off
	ds_read_b32 v162, v217
	s_mov_b32 m0, s46
	s_waitcnt lgkmcnt(0)
	v_lshl_add_u32 v162, v162, 10, v176
	global_load_lds_dwordx4 v162, s[16:17]
	ds_read_b32 v162, v217 offset:256
	s_mov_b32 m0, s47
	s_waitcnt lgkmcnt(0)
	v_lshl_add_u32 v162, v162, 10, v176
	global_load_lds_dwordx4 v162, s[16:17]
	s_waitcnt vmcnt(8)
	s_waitcnt lgkmcnt(0)
	s_setprio 1
	s_barrier
	v_mfma_f32_16x16x128_f8f6f4 v[90:93], v[18:25], v[218:225], v[90:93]
	v_mfma_f32_16x16x128_f8f6f4 v[82:85], v[26:33], v[218:225], v[82:85]
	v_mfma_f32_16x16x128_f8f6f4 v[74:77], v[18:25], v[226:233], v[74:77]
	v_mfma_f32_16x16x128_f8f6f4 v[66:69], v[26:33], v[226:233], v[66:69]
	v_mfma_f32_16x16x128_f8f6f4 v[58:61], v[18:25], v[234:241], v[58:61]
	v_mfma_f32_16x16x128_f8f6f4 v[50:53], v[26:33], v[234:241], v[50:53]
	v_mfma_f32_16x16x128_f8f6f4 v[42:45], v[18:25], v[242:249], v[42:45]
	v_mfma_f32_16x16x128_f8f6f4 v[34:37], v[26:33], v[242:249], v[34:37]
	s_setprio 0
	s_setprio 1
	v_mfma_f32_16x16x128_f8f6f4 v[94:97], v[2:9], v[218:225], v[94:97]
	v_mfma_f32_16x16x128_f8f6f4 v[86:89], v[10:17], v[218:225], v[86:89]
	v_mfma_f32_16x16x128_f8f6f4 v[78:81], v[2:9], v[226:233], v[78:81]
	v_mfma_f32_16x16x128_f8f6f4 v[70:73], v[10:17], v[226:233], v[70:73]
	v_mfma_f32_16x16x128_f8f6f4 v[62:65], v[2:9], v[234:241], v[62:65]
	v_mfma_f32_16x16x128_f8f6f4 v[54:57], v[10:17], v[234:241], v[54:57]
	v_mfma_f32_16x16x128_f8f6f4 v[46:49], v[2:9], v[242:249], v[46:49]
	v_mfma_f32_16x16x128_f8f6f4 v[38:41], v[10:17], v[242:249], v[38:41]
	s_setprio 0
	s_barrier
	s_add_u32 s58, s26, 0x200
	s_addc_u32 s59, s27, 0
	s_mov_b32 s60, 0
	s_mov_b64 s[26:27], 0
.LBB0_1304:
	ds_read_b128 v[2:5], v200
	ds_read_b128 v[6:9], v201
	ds_read_b128 v[10:13], v202
	ds_read_b128 v[14:17], v203
	ds_read_b128 v[18:21], v204
	ds_read_b128 v[22:25], v205
	ds_read_b128 v[26:29], v206
	ds_read_b128 v[30:33], v207
	s_add_u32 s61, s58, s26
	s_addc_u32 s62, s59, s27
	s_add_i32 s63, s26, 0x200
	s_cmp_eq_u32 s60, 4
	s_cselect_b64 s[30:31], -1, 0
	s_and_b64 s[28:29], s[30:31], exec
	s_cselect_b32 s29, s23, s62
	s_cselect_b32 s28, s22, s61
	s_cselect_b32 s61, 0, s63
	s_and_b64 s[30:31], s[24:25], s[30:31]
	ds_read_b128 v[218:221], v216
	ds_read_b128 v[222:225], v216 offset:1024
	ds_read_b128 v[226:229], v216 offset:2048
	ds_read_b128 v[230:233], v216 offset:3072
	ds_read_b32 v162, v217 offset:512
	ds_read_b128 v[234:237], v216 offset:4096
	ds_read_b128 v[238:241], v216 offset:5120
	ds_read_b128 v[242:245], v216 offset:6144
	ds_read_b128 v[246:249], v216 offset:7168
	s_add_u32 s62, s16, s26
	s_waitcnt lgkmcnt(0)
	v_lshl_add_u32 v162, v162, 10, v176
	s_addc_u32 s63, s17, s27
	s_mov_b32 m0, s21
	s_nop 0
	global_load_lds_dwordx4 v162, s[62:63]
	ds_read_b32 v162, v217 offset:768
	s_mov_b32 m0, s57
	s_waitcnt lgkmcnt(0)
	v_lshl_add_u32 v162, v162, 10, v176
	global_load_lds_dwordx4 v162, s[62:63]
	s_waitcnt vmcnt(8)
	s_waitcnt lgkmcnt(0)
	s_setprio 1
	s_barrier
	v_mfma_f32_16x16x128_f8f6f4 v[154:157], v[2:9], v[218:225], v[154:157]
	v_mfma_f32_16x16x128_f8f6f4 v[146:149], v[10:17], v[218:225], v[146:149]
	v_mfma_f32_16x16x128_f8f6f4 v[138:141], v[2:9], v[226:233], v[138:141]
	v_mfma_f32_16x16x128_f8f6f4 v[130:133], v[10:17], v[226:233], v[130:133]
	v_mfma_f32_16x16x128_f8f6f4 v[122:125], v[2:9], v[234:241], v[122:125]
	v_mfma_f32_16x16x128_f8f6f4 v[114:117], v[10:17], v[234:241], v[114:117]
	v_mfma_f32_16x16x128_f8f6f4 v[106:109], v[2:9], v[242:249], v[106:109]
	v_mfma_f32_16x16x128_f8f6f4 v[98:101], v[10:17], v[242:249], v[98:101]
	s_setprio 0
	s_setprio 1
	v_mfma_f32_16x16x128_f8f6f4 v[158:161], v[18:25], v[218:225], v[158:161]
	v_mfma_f32_16x16x128_f8f6f4 v[150:153], v[26:33], v[218:225], v[150:153]
	v_mfma_f32_16x16x128_f8f6f4 v[142:145], v[18:25], v[226:233], v[142:145]
	v_mfma_f32_16x16x128_f8f6f4 v[134:137], v[26:33], v[226:233], v[134:137]
	v_mfma_f32_16x16x128_f8f6f4 v[126:129], v[18:25], v[234:241], v[126:129]
	v_mfma_f32_16x16x128_f8f6f4 v[118:121], v[26:33], v[234:241], v[118:121]
	v_mfma_f32_16x16x128_f8f6f4 v[110:113], v[18:25], v[242:249], v[110:113]
	v_mfma_f32_16x16x128_f8f6f4 v[102:105], v[26:33], v[242:249], v[102:105]
	s_setprio 0
	s_barrier
	s_mov_b32 m0, s37
	v_lshl_add_u64 v[172:173], s[28:29], 0, v[164:165]
	s_add_u32 s62, s28, 0x20000
	ds_read_b128 v[218:221], v216 offset:16384
	ds_read_b128 v[222:225], v216 offset:17408
	ds_read_b128 v[226:229], v216 offset:18432
	ds_read_b128 v[230:233], v216 offset:19456
	ds_read_b128 v[234:237], v216 offset:20480
	ds_read_b128 v[238:241], v216 offset:21504
	ds_read_b128 v[242:245], v216 offset:22528
	ds_read_b128 v[246:249], v216 offset:23552
	global_load_lds_dwordx4 v[172:173], off
	v_lshl_add_u64 v[174:175], s[28:29], 0, v[166:167]
	s_mov_b32 m0, s38
	s_addc_u32 s63, s29, 0
	global_load_lds_dwordx4 v[174:175], off
	v_lshl_add_u64 v[250:251], s[62:63], 0, v[164:165]
	s_mov_b32 m0, s39
	s_and_b64 s[30:31], s[30:31], exec
	global_load_lds_dwordx4 v[250:251], off
	v_lshl_add_u64 v[250:251], s[62:63], 0, v[166:167]
	s_mov_b32 m0, s40
	s_cselect_b32 s30, s53, s56
	global_load_lds_dwordx4 v[250:251], off
	v_lshl_add_u32 v250, s30, 10, v177
	ds_read_b32 v162, v250
	s_add_u32 s30, s6, s61
	s_addc_u32 s31, s7, 0
	s_mov_b32 m0, s36
	s_waitcnt lgkmcnt(0)
	v_lshl_add_u32 v162, v162, 10, v176
	global_load_lds_dwordx4 v162, s[30:31]
	ds_read_b32 v162, v250 offset:256
	s_mov_b32 m0, s41
	s_waitcnt lgkmcnt(0)
	v_lshl_add_u32 v162, v162, 10, v176
	global_load_lds_dwordx4 v162, s[30:31]
	s_waitcnt vmcnt(8)
	s_waitcnt lgkmcnt(0)
	s_setprio 1
	s_barrier
	v_mfma_f32_16x16x128_f8f6f4 v[90:93], v[2:9], v[218:225], v[90:93]
	v_mfma_f32_16x16x128_f8f6f4 v[82:85], v[10:17], v[218:225], v[82:85]
	v_mfma_f32_16x16x128_f8f6f4 v[74:77], v[2:9], v[226:233], v[74:77]
	v_mfma_f32_16x16x128_f8f6f4 v[66:69], v[10:17], v[226:233], v[66:69]
	v_mfma_f32_16x16x128_f8f6f4 v[58:61], v[2:9], v[234:241], v[58:61]
	v_mfma_f32_16x16x128_f8f6f4 v[50:53], v[10:17], v[234:241], v[50:53]
	v_mfma_f32_16x16x128_f8f6f4 v[42:45], v[2:9], v[242:249], v[42:45]
	v_mfma_f32_16x16x128_f8f6f4 v[34:37], v[10:17], v[242:249], v[34:37]
	s_setprio 0
	s_setprio 1
	v_mfma_f32_16x16x128_f8f6f4 v[94:97], v[18:25], v[218:225], v[94:97]
	v_mfma_f32_16x16x128_f8f6f4 v[86:89], v[26:33], v[218:225], v[86:89]
	v_mfma_f32_16x16x128_f8f6f4 v[78:81], v[18:25], v[226:233], v[78:81]
	v_mfma_f32_16x16x128_f8f6f4 v[70:73], v[26:33], v[226:233], v[70:73]
	v_mfma_f32_16x16x128_f8f6f4 v[62:65], v[18:25], v[234:241], v[62:65]
	v_mfma_f32_16x16x128_f8f6f4 v[54:57], v[26:33], v[234:241], v[54:57]
	v_mfma_f32_16x16x128_f8f6f4 v[46:49], v[18:25], v[242:249], v[46:49]
	v_mfma_f32_16x16x128_f8f6f4 v[38:41], v[26:33], v[242:249], v[38:41]
	s_setprio 0
	s_barrier
	ds_read_b128 v[10:13], v208
	ds_read_b128 v[14:17], v209
	ds_read_b128 v[26:29], v210
	ds_read_b128 v[30:33], v211
	ds_read_b128 v[2:5], v212
	ds_read_b128 v[6:9], v213
	ds_read_b128 v[18:21], v214
	ds_read_b128 v[22:25], v215
	ds_read_b128 v[218:221], v216 offset:32768
	ds_read_b128 v[222:225], v216 offset:33792
	ds_read_b128 v[226:229], v216 offset:34816
	ds_read_b128 v[230:233], v216 offset:35840
	ds_read_b32 v162, v250 offset:512
	ds_read_b128 v[234:237], v216 offset:36864
	ds_read_b128 v[238:241], v216 offset:37888
	ds_read_b128 v[242:245], v216 offset:38912
	ds_read_b128 v[246:249], v216 offset:39936
	s_waitcnt lgkmcnt(0)
	v_lshl_add_u32 v162, v162, 10, v176
	s_mov_b32 m0, s42
	s_nop 0
	global_load_lds_dwordx4 v162, s[30:31]
	ds_read_b32 v162, v250 offset:768
	s_mov_b32 m0, s43
	s_waitcnt lgkmcnt(0)
	v_lshl_add_u32 v162, v162, 10, v176
	global_load_lds_dwordx4 v162, s[30:31]
	s_waitcnt vmcnt(8)
	s_waitcnt lgkmcnt(0)
	s_setprio 1
	s_barrier
	v_mfma_f32_16x16x128_f8f6f4 v[154:157], v[10:17], v[218:225], v[154:157]
	v_mfma_f32_16x16x128_f8f6f4 v[146:149], v[26:33], v[218:225], v[146:149]
	v_mfma_f32_16x16x128_f8f6f4 v[138:141], v[10:17], v[226:233], v[138:141]
	v_mfma_f32_16x16x128_f8f6f4 v[130:133], v[26:33], v[226:233], v[130:133]
	v_mfma_f32_16x16x128_f8f6f4 v[122:125], v[10:17], v[234:241], v[122:125]
	v_mfma_f32_16x16x128_f8f6f4 v[114:117], v[26:33], v[234:241], v[114:117]
	v_mfma_f32_16x16x128_f8f6f4 v[106:109], v[10:17], v[242:249], v[106:109]
	v_mfma_f32_16x16x128_f8f6f4 v[98:101], v[26:33], v[242:249], v[98:101]
	s_setprio 0
	s_setprio 1
	v_mfma_f32_16x16x128_f8f6f4 v[158:161], v[2:9], v[218:225], v[158:161]
	v_mfma_f32_16x16x128_f8f6f4 v[150:153], v[18:25], v[218:225], v[150:153]
	v_mfma_f32_16x16x128_f8f6f4 v[142:145], v[2:9], v[226:233], v[142:145]
	v_mfma_f32_16x16x128_f8f6f4 v[134:137], v[18:25], v[226:233], v[134:137]
	v_mfma_f32_16x16x128_f8f6f4 v[126:129], v[2:9], v[234:241], v[126:129]
	v_mfma_f32_16x16x128_f8f6f4 v[118:121], v[18:25], v[234:241], v[118:121]
	v_mfma_f32_16x16x128_f8f6f4 v[110:113], v[2:9], v[242:249], v[110:113]
	v_mfma_f32_16x16x128_f8f6f4 v[102:105], v[18:25], v[242:249], v[102:105]
	s_setprio 0
	s_barrier
	s_mov_b32 m0, s44
	v_lshl_add_u64 v[172:173], v[172:173], 0, s[90:91]
	s_add_u32 s28, s28, 0x20080
	ds_read_b128 v[218:221], v216 offset:49152
	ds_read_b128 v[222:225], v216 offset:50176
	ds_read_b128 v[226:229], v216 offset:51200
	ds_read_b128 v[230:233], v216 offset:52224
	ds_read_b128 v[234:237], v216 offset:53248
	ds_read_b128 v[238:241], v216 offset:54272
	ds_read_b128 v[242:245], v216 offset:55296
	ds_read_b128 v[246:249], v216 offset:56320
	global_load_lds_dwordx4 v[172:173], off
	v_lshl_add_u64 v[172:173], v[174:175], 0, s[90:91]
	s_mov_b32 m0, s45
	s_addc_u32 s29, s29, 0
	global_load_lds_dwordx4 v[172:173], off
	v_lshl_add_u64 v[172:173], s[28:29], 0, v[164:165]
	s_mov_b32 m0, s48
	s_nop 0
	global_load_lds_dwordx4 v[172:173], off
	v_lshl_add_u64 v[172:173], s[28:29], 0, v[166:167]
	s_mov_b32 m0, s49
	s_nop 0
	global_load_lds_dwordx4 v[172:173], off
	ds_read_b32 v162, v250
	s_mov_b32 m0, s46
	s_waitcnt lgkmcnt(0)
	v_lshl_add_u32 v162, v162, 10, v176
	v_lshl_add_u64 v[172:173], s[30:31], 0, v[162:163]
	v_lshl_add_u64 v[172:173], v[172:173], 0, s[90:91]
	global_load_lds_dwordx4 v[172:173], off
	ds_read_b32 v162, v250 offset:256
	s_mov_b32 m0, s47
	s_waitcnt lgkmcnt(0)
	v_lshl_add_u32 v162, v162, 10, v176
	v_lshl_add_u64 v[172:173], s[30:31], 0, v[162:163]
	v_lshl_add_u64 v[172:173], v[172:173], 0, s[90:91]
	global_load_lds_dwordx4 v[172:173], off
	s_waitcnt vmcnt(8)
	s_waitcnt lgkmcnt(0)
	s_setprio 1
	s_barrier
	v_mfma_f32_16x16x128_f8f6f4 v[90:93], v[10:17], v[218:225], v[90:93]
	v_mfma_f32_16x16x128_f8f6f4 v[82:85], v[26:33], v[218:225], v[82:85]
	v_mfma_f32_16x16x128_f8f6f4 v[74:77], v[10:17], v[226:233], v[74:77]
	v_mfma_f32_16x16x128_f8f6f4 v[66:69], v[26:33], v[226:233], v[66:69]
	v_mfma_f32_16x16x128_f8f6f4 v[58:61], v[10:17], v[234:241], v[58:61]
	v_mfma_f32_16x16x128_f8f6f4 v[50:53], v[26:33], v[234:241], v[50:53]
	v_mfma_f32_16x16x128_f8f6f4 v[42:45], v[10:17], v[242:249], v[42:45]
	v_mfma_f32_16x16x128_f8f6f4 v[34:37], v[26:33], v[242:249], v[34:37]
	s_setprio 0
	s_setprio 1
	v_mfma_f32_16x16x128_f8f6f4 v[94:97], v[2:9], v[218:225], v[94:97]
	v_mfma_f32_16x16x128_f8f6f4 v[86:89], v[18:25], v[218:225], v[86:89]
	v_mfma_f32_16x16x128_f8f6f4 v[78:81], v[2:9], v[226:233], v[78:81]
	v_mfma_f32_16x16x128_f8f6f4 v[70:73], v[18:25], v[226:233], v[70:73]
	v_mfma_f32_16x16x128_f8f6f4 v[62:65], v[2:9], v[234:241], v[62:65]
	v_mfma_f32_16x16x128_f8f6f4 v[54:57], v[18:25], v[234:241], v[54:57]
	v_mfma_f32_16x16x128_f8f6f4 v[46:49], v[2:9], v[242:249], v[46:49]
	v_mfma_f32_16x16x128_f8f6f4 v[38:41], v[18:25], v[242:249], v[38:41]
	s_setprio 0
	s_barrier
	s_add_i32 s60, s60, 2
	s_add_u32 s26, s26, 0x100
	s_addc_u32 s27, s27, 0
	s_cmp_lt_u32 s60, 6
	s_cbranch_scc1 .LBB0_1304
	s_andn2_b64 vcc, exec, s[18:19]
	s_cbranch_vccnz .LBB0_1307
	s_barrier

.LBB0_1373:
	ds_read_b128 v[2:5], v202
	ds_read_b128 v[6:9], v203
	ds_read_b128 v[10:13], v204
	ds_read_b128 v[14:17], v205
	ds_read_b128 v[18:21], v206
	ds_read_b128 v[22:25], v207
	ds_read_b128 v[26:29], v208
	ds_read_b128 v[30:33], v209
	s_ashr_i32 s13, s12, 31
	s_lshl_b64 s[16:17], s[12:13], 19
	s_add_u32 s16, s27, s16
	s_addc_u32 s17, s28, s17
	s_and_b64 s[24:25], s[24:25], exec
	s_cselect_b32 s11, s17, s23
	s_cselect_b32 s13, s16, s22
	s_add_u32 s24, s22, 0x40080
	s_addc_u32 s25, s23, 0
	s_add_i32 s47, s31, 0xc000
	v_lshl_add_u64 v[66:67], s[24:25], 0, v[162:163]
	s_mov_b32 m0, s47
	s_add_i32 s48, s31, 0xe000
	ds_read_b128 v[34:37], v218
	ds_read_b128 v[38:41], v218 offset:1024
	ds_read_b128 v[42:45], v218 offset:2048
	ds_read_b128 v[46:49], v218 offset:3072
	ds_read_b128 v[50:53], v218 offset:4096
	ds_read_b128 v[54:57], v218 offset:5120
	ds_read_b128 v[58:61], v218 offset:6144
	ds_read_b128 v[62:65], v218 offset:7168
	global_load_lds_dwordx4 v[66:67], off
	v_lshl_add_u64 v[66:67], s[24:25], 0, v[164:165]
	s_mov_b32 m0, s48
	s_nop 0
	global_load_lds_dwordx4 v[66:67], off
	s_waitcnt vmcnt(8)
	s_waitcnt lgkmcnt(0)
	s_setprio 1
	s_barrier
	v_mfma_f32_16x16x128_f8f6f4 v[158:161], v[2:9], v[34:41], 0
	v_mfma_f32_16x16x128_f8f6f4 v[154:157], v[10:17], v[34:41], 0
	v_mfma_f32_16x16x128_f8f6f4 v[150:153], v[2:9], v[42:49], 0
	v_mfma_f32_16x16x128_f8f6f4 v[146:149], v[10:17], v[42:49], 0
	v_mfma_f32_16x16x128_f8f6f4 v[126:129], v[2:9], v[50:57], 0
	v_mfma_f32_16x16x128_f8f6f4 v[122:125], v[10:17], v[50:57], 0
	v_mfma_f32_16x16x128_f8f6f4 v[118:121], v[2:9], v[58:65], 0
	v_mfma_f32_16x16x128_f8f6f4 v[114:117], v[10:17], v[58:65], 0
	s_setprio 0
	s_setprio 1
	v_mfma_f32_16x16x128_f8f6f4 v[142:145], v[18:25], v[34:41], 0
	v_mfma_f32_16x16x128_f8f6f4 v[138:141], v[26:33], v[34:41], 0
	v_mfma_f32_16x16x128_f8f6f4 v[134:137], v[18:25], v[42:49], 0
	v_mfma_f32_16x16x128_f8f6f4 v[130:133], v[26:33], v[42:49], 0
	v_mfma_f32_16x16x128_f8f6f4 v[110:113], v[18:25], v[50:57], 0
	v_mfma_f32_16x16x128_f8f6f4 v[106:109], v[26:33], v[50:57], 0
	v_mfma_f32_16x16x128_f8f6f4 v[98:101], v[18:25], v[58:65], 0
	v_mfma_f32_16x16x128_f8f6f4 v[90:93], v[26:33], v[58:65], 0
	s_setprio 0
	s_barrier
	v_lshl_add_u64 v[172:173], s[20:21], 0, v[162:163]
	s_mov_b64 s[50:51], 0x100
	s_mov_b32 m0, s33
	v_lshl_add_u64 v[50:51], v[172:173], 0, s[50:51]
	v_lshl_add_u64 v[174:175], s[20:21], 0, v[164:165]
	s_add_u32 s24, s20, 0x40100
	ds_read_b128 v[34:37], v218 offset:16384
	ds_read_b128 v[38:41], v218 offset:17408
	ds_read_b128 v[42:45], v218 offset:18432
	ds_read_b128 v[46:49], v218 offset:19456
	ds_read_b128 v[220:223], v218 offset:20480
	ds_read_b128 v[224:227], v218 offset:21504
	ds_read_b128 v[228:231], v218 offset:22528
	ds_read_b128 v[232:235], v218 offset:23552
	global_load_lds_dwordx4 v[50:51], off
	v_lshl_add_u64 v[50:51], v[174:175], 0, s[50:51]
	s_mov_b32 m0, s34
	s_addc_u32 s25, s21, 0
	global_load_lds_dwordx4 v[50:51], off
	v_lshl_add_u64 v[50:51], s[24:25], 0, v[162:163]
	s_mov_b32 m0, s35
	v_lshl_add_u64 v[176:177], s[22:23], 0, v[162:163]
	global_load_lds_dwordx4 v[50:51], off
	v_lshl_add_u64 v[50:51], s[24:25], 0, v[164:165]
	s_mov_b32 m0, s36
	v_lshl_add_u64 v[178:179], s[22:23], 0, v[164:165]
	global_load_lds_dwordx4 v[50:51], off
	v_lshl_add_u64 v[50:51], v[176:177], 0, s[50:51]
	s_mov_b32 m0, s31
	s_nop 0
	global_load_lds_dwordx4 v[50:51], off
	v_lshl_add_u64 v[50:51], v[178:179], 0, s[50:51]
	s_mov_b32 m0, s37
	s_nop 0
	global_load_lds_dwordx4 v[50:51], off
	s_waitcnt vmcnt(8)
	s_waitcnt lgkmcnt(0)
	s_setprio 1
	s_barrier
	v_mfma_f32_16x16x128_f8f6f4 v[102:105], v[2:9], v[34:41], 0
	v_mfma_f32_16x16x128_f8f6f4 v[94:97], v[10:17], v[34:41], 0
	v_mfma_f32_16x16x128_f8f6f4 v[86:89], v[2:9], v[42:49], 0
	v_mfma_f32_16x16x128_f8f6f4 v[82:85], v[10:17], v[42:49], 0
	v_mfma_f32_16x16x128_f8f6f4 v[62:65], v[2:9], v[220:227], 0
	v_mfma_f32_16x16x128_f8f6f4 v[58:61], v[10:17], v[220:227], 0
	v_mfma_f32_16x16x128_f8f6f4 v[54:57], v[2:9], v[228:235], 0
	v_mfma_f32_16x16x128_f8f6f4 v[50:53], v[10:17], v[228:235], 0
	s_setprio 0
	s_setprio 1
	v_mfma_f32_16x16x128_f8f6f4 v[78:81], v[18:25], v[34:41], 0
	v_mfma_f32_16x16x128_f8f6f4 v[74:77], v[26:33], v[34:41], 0
	v_mfma_f32_16x16x128_f8f6f4 v[70:73], v[18:25], v[42:49], 0
	v_mfma_f32_16x16x128_f8f6f4 v[66:69], v[26:33], v[42:49], 0
	v_mfma_f32_16x16x128_f8f6f4 v[46:49], v[18:25], v[220:227], 0
	v_mfma_f32_16x16x128_f8f6f4 v[42:45], v[26:33], v[220:227], 0
	v_mfma_f32_16x16x128_f8f6f4 v[38:41], v[18:25], v[228:235], 0
	v_mfma_f32_16x16x128_f8f6f4 v[34:37], v[26:33], v[228:235], 0
	s_setprio 0
	s_barrier
	ds_read_b128 v[18:21], v210
	ds_read_b128 v[22:25], v211
	ds_read_b128 v[26:29], v212
	ds_read_b128 v[30:33], v213
	ds_read_b128 v[2:5], v214
	ds_read_b128 v[6:9], v215
	ds_read_b128 v[10:13], v216
	ds_read_b128 v[14:17], v217
	s_add_u32 s24, s22, 0x40100
	s_addc_u32 s25, s23, 0
	s_mov_b32 m0, s38
	v_lshl_add_u64 v[252:253], s[24:25], 0, v[162:163]
	ds_read_b128 v[220:223], v218 offset:32768
	ds_read_b128 v[224:227], v218 offset:33792
	ds_read_b128 v[228:231], v218 offset:34816
	ds_read_b128 v[232:235], v218 offset:35840
	ds_read_b128 v[236:239], v218 offset:36864
	ds_read_b128 v[240:243], v218 offset:37888
	ds_read_b128 v[244:247], v218 offset:38912
	ds_read_b128 v[248:251], v218 offset:39936
	global_load_lds_dwordx4 v[252:253], off
	v_lshl_add_u64 v[252:253], s[24:25], 0, v[164:165]
	s_mov_b32 m0, s39
	s_nop 0
	global_load_lds_dwordx4 v[252:253], off
	s_waitcnt vmcnt(8)
	s_waitcnt lgkmcnt(0)
	s_setprio 1
	s_barrier
	v_mfma_f32_16x16x128_f8f6f4 v[158:161], v[18:25], v[220:227], v[158:161]
	v_mfma_f32_16x16x128_f8f6f4 v[154:157], v[26:33], v[220:227], v[154:157]
	v_mfma_f32_16x16x128_f8f6f4 v[150:153], v[18:25], v[228:235], v[150:153]
	v_mfma_f32_16x16x128_f8f6f4 v[146:149], v[26:33], v[228:235], v[146:149]
	v_mfma_f32_16x16x128_f8f6f4 v[126:129], v[18:25], v[236:243], v[126:129]
	v_mfma_f32_16x16x128_f8f6f4 v[122:125], v[26:33], v[236:243], v[122:125]
	v_mfma_f32_16x16x128_f8f6f4 v[118:121], v[18:25], v[244:251], v[118:121]
	v_mfma_f32_16x16x128_f8f6f4 v[114:117], v[26:33], v[244:251], v[114:117]
	s_setprio 0
	s_setprio 1
	v_mfma_f32_16x16x128_f8f6f4 v[142:145], v[2:9], v[220:227], v[142:145]
	v_mfma_f32_16x16x128_f8f6f4 v[138:141], v[10:17], v[220:227], v[138:141]
	v_mfma_f32_16x16x128_f8f6f4 v[134:137], v[2:9], v[228:235], v[134:137]
	v_mfma_f32_16x16x128_f8f6f4 v[130:133], v[10:17], v[228:235], v[130:133]
	v_mfma_f32_16x16x128_f8f6f4 v[110:113], v[2:9], v[236:243], v[110:113]
	v_mfma_f32_16x16x128_f8f6f4 v[106:109], v[10:17], v[236:243], v[106:109]
	v_mfma_f32_16x16x128_f8f6f4 v[98:101], v[2:9], v[244:251], v[98:101]
	v_mfma_f32_16x16x128_f8f6f4 v[90:93], v[10:17], v[244:251], v[90:93]
	s_setprio 0
	s_barrier
	s_mov_b64 s[50:51], 0x180
	s_mov_b32 m0, s40
	v_lshl_add_u64 v[172:173], v[172:173], 0, s[50:51]
	s_add_u32 s24, s20, 0x40180
	ds_read_b128 v[220:223], v218 offset:49152
	ds_read_b128 v[224:227], v218 offset:50176
	ds_read_b128 v[228:231], v218 offset:51200
	ds_read_b128 v[232:235], v218 offset:52224
	ds_read_b128 v[236:239], v218 offset:53248
	ds_read_b128 v[240:243], v218 offset:54272
	ds_read_b128 v[244:247], v218 offset:55296
	ds_read_b128 v[248:251], v218 offset:56320
	global_load_lds_dwordx4 v[172:173], off
	v_lshl_add_u64 v[172:173], v[174:175], 0, s[50:51]
	s_mov_b32 m0, s41
	s_addc_u32 s25, s21, 0
	global_load_lds_dwordx4 v[172:173], off
	v_lshl_add_u64 v[172:173], s[24:25], 0, v[162:163]
	s_mov_b32 m0, s44
	s_nop 0
	global_load_lds_dwordx4 v[172:173], off
	v_lshl_add_u64 v[172:173], s[24:25], 0, v[164:165]
	s_mov_b32 m0, s45
	s_nop 0
	global_load_lds_dwordx4 v[172:173], off
	v_lshl_add_u64 v[172:173], v[176:177], 0, s[50:51]
	s_mov_b32 m0, s42
	s_nop 0
	global_load_lds_dwordx4 v[172:173], off
	v_lshl_add_u64 v[172:173], v[178:179], 0, s[50:51]
	s_mov_b32 m0, s43
	s_nop 0
	global_load_lds_dwordx4 v[172:173], off
	s_waitcnt vmcnt(8)
	s_waitcnt lgkmcnt(0)
	s_setprio 1
	s_barrier
	v_mfma_f32_16x16x128_f8f6f4 v[102:105], v[18:25], v[220:227], v[102:105]
	v_mfma_f32_16x16x128_f8f6f4 v[94:97], v[26:33], v[220:227], v[94:97]
	v_mfma_f32_16x16x128_f8f6f4 v[86:89], v[18:25], v[228:235], v[86:89]
	v_mfma_f32_16x16x128_f8f6f4 v[82:85], v[26:33], v[228:235], v[82:85]
	v_mfma_f32_16x16x128_f8f6f4 v[62:65], v[18:25], v[236:243], v[62:65]
	v_mfma_f32_16x16x128_f8f6f4 v[58:61], v[26:33], v[236:243], v[58:61]
	v_mfma_f32_16x16x128_f8f6f4 v[54:57], v[18:25], v[244:251], v[54:57]
	v_mfma_f32_16x16x128_f8f6f4 v[50:53], v[26:33], v[244:251], v[50:53]
	s_setprio 0
	s_setprio 1
	v_mfma_f32_16x16x128_f8f6f4 v[78:81], v[2:9], v[220:227], v[78:81]
	v_mfma_f32_16x16x128_f8f6f4 v[74:77], v[10:17], v[220:227], v[74:77]
	v_mfma_f32_16x16x128_f8f6f4 v[70:73], v[2:9], v[228:235], v[70:73]
	v_mfma_f32_16x16x128_f8f6f4 v[66:69], v[10:17], v[228:235], v[66:69]
	v_mfma_f32_16x16x128_f8f6f4 v[46:49], v[2:9], v[236:243], v[46:49]
	v_mfma_f32_16x16x128_f8f6f4 v[42:45], v[10:17], v[236:243], v[42:45]
	v_mfma_f32_16x16x128_f8f6f4 v[38:41], v[2:9], v[244:251], v[38:41]
	v_mfma_f32_16x16x128_f8f6f4 v[34:37], v[10:17], v[244:251], v[34:37]
	s_setprio 0
	s_barrier
	s_add_u32 s49, s20, 0x200
	s_addc_u32 s50, s21, 0
	s_add_u32 s20, s22, 0x40180
	s_addc_u32 s21, s23, 0
	s_mov_b32 s51, 0
.LBB0_1374:
	ds_read_b128 v[2:5], v202
	ds_read_b128 v[6:9], v203
	ds_read_b128 v[18:21], v204
	ds_read_b128 v[22:25], v205
	ds_read_b128 v[26:29], v206
	ds_read_b128 v[30:33], v207
	ds_read_b128 v[172:175], v208
	ds_read_b128 v[176:179], v209
	s_add_u32 s22, s20, 0xfffc0080
	s_addc_u32 s23, s21, -1
	s_cmp_eq_u32 s51, 12
	s_cselect_b32 s25, s11, s23
	s_cselect_b32 s24, s13, s22
	s_cselect_b32 s23, s15, s50
	s_cselect_b32 s22, s14, s49
	s_mov_b32 m0, s47
	v_lshl_add_u64 v[244:245], s[20:21], 0, v[170:171]
	ds_read_b128 v[10:13], v218
	ds_read_b128 v[14:17], v218 offset:1024
	ds_read_b128 v[220:223], v218 offset:2048
	ds_read_b128 v[224:227], v218 offset:3072
	ds_read_b128 v[228:231], v218 offset:4096
	ds_read_b128 v[232:235], v218 offset:5120
	ds_read_b128 v[236:239], v218 offset:6144
	ds_read_b128 v[240:243], v218 offset:7168
	global_load_lds_dwordx4 v[244:245], off
	v_lshl_add_u64 v[244:245], s[20:21], 0, v[168:169]
	s_mov_b32 m0, s48
	s_nop 0
	global_load_lds_dwordx4 v[244:245], off
	s_waitcnt vmcnt(8)
	s_waitcnt lgkmcnt(0)
	s_setprio 1
	s_barrier
	v_mfma_f32_16x16x128_f8f6f4 v[158:161], v[2:9], v[10:17], v[158:161]
	v_mfma_f32_16x16x128_f8f6f4 v[154:157], v[18:25], v[10:17], v[154:157]
	v_mfma_f32_16x16x128_f8f6f4 v[150:153], v[2:9], v[220:227], v[150:153]
	v_mfma_f32_16x16x128_f8f6f4 v[146:149], v[18:25], v[220:227], v[146:149]
	v_mfma_f32_16x16x128_f8f6f4 v[126:129], v[2:9], v[228:235], v[126:129]
	v_mfma_f32_16x16x128_f8f6f4 v[122:125], v[18:25], v[228:235], v[122:125]
	v_mfma_f32_16x16x128_f8f6f4 v[118:121], v[2:9], v[236:243], v[118:121]
	v_mfma_f32_16x16x128_f8f6f4 v[114:117], v[18:25], v[236:243], v[114:117]
	s_setprio 0
	s_setprio 1
	v_mfma_f32_16x16x128_f8f6f4 v[142:145], v[26:33], v[10:17], v[142:145]
	v_mfma_f32_16x16x128_f8f6f4 v[138:141], v[172:179], v[10:17], v[138:141]
	v_mfma_f32_16x16x128_f8f6f4 v[134:137], v[26:33], v[220:227], v[134:137]
	v_mfma_f32_16x16x128_f8f6f4 v[130:133], v[172:179], v[220:227], v[130:133]
	v_mfma_f32_16x16x128_f8f6f4 v[110:113], v[26:33], v[228:235], v[110:113]
	v_mfma_f32_16x16x128_f8f6f4 v[106:109], v[172:179], v[228:235], v[106:109]
	v_mfma_f32_16x16x128_f8f6f4 v[98:101], v[26:33], v[236:243], v[98:101]
	v_mfma_f32_16x16x128_f8f6f4 v[90:93], v[172:179], v[236:243], v[90:93]
	s_setprio 0
	s_barrier
	s_mov_b32 m0, s33
	v_lshl_add_u64 v[10:11], s[22:23], 0, v[162:163]
	s_add_u32 s52, s22, 0x40000
	ds_read_b128 v[220:223], v218 offset:16384
	ds_read_b128 v[224:227], v218 offset:17408
	ds_read_b128 v[228:231], v218 offset:18432
	ds_read_b128 v[232:235], v218 offset:19456
	ds_read_b128 v[236:239], v218 offset:20480
	ds_read_b128 v[240:243], v218 offset:21504
	ds_read_b128 v[244:247], v218 offset:22528
	ds_read_b128 v[248:251], v218 offset:23552
	global_load_lds_dwordx4 v[10:11], off
	v_lshl_add_u64 v[12:13], s[22:23], 0, v[164:165]
	s_mov_b32 m0, s34
	s_addc_u32 s53, s23, 0
	global_load_lds_dwordx4 v[12:13], off
	v_lshl_add_u64 v[14:15], s[52:53], 0, v[162:163]
	s_mov_b32 m0, s35
	v_lshl_add_u64 v[16:17], s[24:25], 0, v[164:165]
	global_load_lds_dwordx4 v[14:15], off
	v_lshl_add_u64 v[14:15], s[52:53], 0, v[164:165]
	s_mov_b32 m0, s36
	s_nop 0
	global_load_lds_dwordx4 v[14:15], off
	v_lshl_add_u64 v[14:15], s[24:25], 0, v[162:163]
	s_mov_b32 m0, s31
	s_nop 0
	global_load_lds_dwordx4 v[14:15], off
	s_mov_b32 m0, s37
	s_nop 0
	global_load_lds_dwordx4 v[16:17], off
	s_waitcnt vmcnt(8)
	s_waitcnt lgkmcnt(0)
	s_setprio 1
	s_barrier
	v_mfma_f32_16x16x128_f8f6f4 v[102:105], v[2:9], v[220:227], v[102:105]
	v_mfma_f32_16x16x128_f8f6f4 v[94:97], v[18:25], v[220:227], v[94:97]
	v_mfma_f32_16x16x128_f8f6f4 v[86:89], v[2:9], v[228:235], v[86:89]
	v_mfma_f32_16x16x128_f8f6f4 v[82:85], v[18:25], v[228:235], v[82:85]
	v_mfma_f32_16x16x128_f8f6f4 v[62:65], v[2:9], v[236:243], v[62:65]
	v_mfma_f32_16x16x128_f8f6f4 v[58:61], v[18:25], v[236:243], v[58:61]
	v_mfma_f32_16x16x128_f8f6f4 v[54:57], v[2:9], v[244:251], v[54:57]
	v_mfma_f32_16x16x128_f8f6f4 v[50:53], v[18:25], v[244:251], v[50:53]
	s_setprio 0
	s_setprio 1
	v_mfma_f32_16x16x128_f8f6f4 v[78:81], v[26:33], v[220:227], v[78:81]
	v_mfma_f32_16x16x128_f8f6f4 v[74:77], v[172:179], v[220:227], v[74:77]
	v_mfma_f32_16x16x128_f8f6f4 v[70:73], v[26:33], v[228:235], v[70:73]
	v_mfma_f32_16x16x128_f8f6f4 v[66:69], v[172:179], v[228:235], v[66:69]
	v_mfma_f32_16x16x128_f8f6f4 v[46:49], v[26:33], v[236:243], v[46:49]
	v_mfma_f32_16x16x128_f8f6f4 v[42:45], v[172:179], v[236:243], v[42:45]
	v_mfma_f32_16x16x128_f8f6f4 v[38:41], v[26:33], v[244:251], v[38:41]
	v_mfma_f32_16x16x128_f8f6f4 v[34:37], v[172:179], v[244:251], v[34:37]
	s_setprio 0
	s_barrier
	ds_read_b128 v[18:21], v210
	ds_read_b128 v[22:25], v211
	ds_read_b128 v[26:29], v212
	ds_read_b128 v[30:33], v213
	ds_read_b128 v[2:5], v214
	ds_read_b128 v[6:9], v215
	ds_read_b128 v[172:175], v216
	ds_read_b128 v[176:179], v217
	s_add_u32 s24, s24, 0x40000
	s_addc_u32 s25, s25, 0
	s_mov_b32 m0, s38
	v_lshl_add_u64 v[252:253], s[24:25], 0, v[162:163]
	ds_read_b128 v[220:223], v218 offset:32768
	ds_read_b128 v[224:227], v218 offset:33792
	ds_read_b128 v[228:231], v218 offset:34816
	ds_read_b128 v[232:235], v218 offset:35840
	ds_read_b128 v[236:239], v218 offset:36864
	ds_read_b128 v[240:243], v218 offset:37888
	ds_read_b128 v[244:247], v218 offset:38912
	ds_read_b128 v[248:251], v218 offset:39936
	global_load_lds_dwordx4 v[252:253], off
	v_lshl_add_u64 v[252:253], s[24:25], 0, v[164:165]
	s_mov_b32 m0, s39
	s_nop 0
	global_load_lds_dwordx4 v[252:253], off
	s_waitcnt vmcnt(8)
	s_waitcnt lgkmcnt(0)
	s_setprio 1
	s_barrier
	v_mfma_f32_16x16x128_f8f6f4 v[158:161], v[18:25], v[220:227], v[158:161]
	v_mfma_f32_16x16x128_f8f6f4 v[154:157], v[26:33], v[220:227], v[154:157]
	v_mfma_f32_16x16x128_f8f6f4 v[150:153], v[18:25], v[228:235], v[150:153]
	v_mfma_f32_16x16x128_f8f6f4 v[146:149], v[26:33], v[228:235], v[146:149]
	v_mfma_f32_16x16x128_f8f6f4 v[126:129], v[18:25], v[236:243], v[126:129]
	v_mfma_f32_16x16x128_f8f6f4 v[122:125], v[26:33], v[236:243], v[122:125]
	v_mfma_f32_16x16x128_f8f6f4 v[118:121], v[18:25], v[244:251], v[118:121]
	v_mfma_f32_16x16x128_f8f6f4 v[114:117], v[26:33], v[244:251], v[114:117]
	s_setprio 0
	s_setprio 1
	v_mfma_f32_16x16x128_f8f6f4 v[142:145], v[2:9], v[220:227], v[142:145]
	v_mfma_f32_16x16x128_f8f6f4 v[138:141], v[172:179], v[220:227], v[138:141]
	v_mfma_f32_16x16x128_f8f6f4 v[134:137], v[2:9], v[228:235], v[134:137]
	v_mfma_f32_16x16x128_f8f6f4 v[130:133], v[172:179], v[228:235], v[130:133]
	v_mfma_f32_16x16x128_f8f6f4 v[110:113], v[2:9], v[236:243], v[110:113]
	v_mfma_f32_16x16x128_f8f6f4 v[106:109], v[172:179], v[236:243], v[106:109]
	v_mfma_f32_16x16x128_f8f6f4 v[98:101], v[2:9], v[244:251], v[98:101]
	v_mfma_f32_16x16x128_f8f6f4 v[90:93], v[172:179], v[244:251], v[90:93]
	s_setprio 0
	s_barrier
	s_mov_b32 m0, s40
	v_lshl_add_u64 v[10:11], v[10:11], 0, s[90:91]
	s_add_u32 s22, s22, 0x40080
	ds_read_b128 v[220:223], v218 offset:49152
	ds_read_b128 v[224:227], v218 offset:50176
	ds_read_b128 v[228:231], v218 offset:51200
	ds_read_b128 v[232:235], v218 offset:52224
	ds_read_b128 v[236:239], v218 offset:53248
	ds_read_b128 v[240:243], v218 offset:54272
	ds_read_b128 v[244:247], v218 offset:55296
	ds_read_b128 v[248:251], v218 offset:56320
	global_load_lds_dwordx4 v[10:11], off
	v_lshl_add_u64 v[10:11], v[12:13], 0, s[90:91]
	s_mov_b32 m0, s41
	s_addc_u32 s23, s23, 0
	global_load_lds_dwordx4 v[10:11], off
	v_lshl_add_u64 v[10:11], s[22:23], 0, v[162:163]
	s_mov_b32 m0, s44
	s_nop 0
	global_load_lds_dwordx4 v[10:11], off
	v_lshl_add_u64 v[10:11], s[22:23], 0, v[164:165]
	s_mov_b32 m0, s45
	s_nop 0
	global_load_lds_dwordx4 v[10:11], off
	v_lshl_add_u64 v[10:11], v[14:15], 0, s[90:91]
	s_mov_b32 m0, s42
	s_nop 0
	global_load_lds_dwordx4 v[10:11], off
	v_lshl_add_u64 v[10:11], v[16:17], 0, s[90:91]
	s_mov_b32 m0, s43
	s_nop 0
	global_load_lds_dwordx4 v[10:11], off
	s_waitcnt vmcnt(8)
	s_waitcnt lgkmcnt(0)
	s_setprio 1
	s_barrier
	v_mfma_f32_16x16x128_f8f6f4 v[102:105], v[18:25], v[220:227], v[102:105]
	v_mfma_f32_16x16x128_f8f6f4 v[94:97], v[26:33], v[220:227], v[94:97]
	v_mfma_f32_16x16x128_f8f6f4 v[86:89], v[18:25], v[228:235], v[86:89]
	v_mfma_f32_16x16x128_f8f6f4 v[82:85], v[26:33], v[228:235], v[82:85]
	v_mfma_f32_16x16x128_f8f6f4 v[62:65], v[18:25], v[236:243], v[62:65]
	v_mfma_f32_16x16x128_f8f6f4 v[58:61], v[26:33], v[236:243], v[58:61]
	v_mfma_f32_16x16x128_f8f6f4 v[54:57], v[18:25], v[244:251], v[54:57]
	v_mfma_f32_16x16x128_f8f6f4 v[50:53], v[26:33], v[244:251], v[50:53]
	s_setprio 0
	s_setprio 1
	v_mfma_f32_16x16x128_f8f6f4 v[78:81], v[2:9], v[220:227], v[78:81]
	v_mfma_f32_16x16x128_f8f6f4 v[74:77], v[172:179], v[220:227], v[74:77]
	v_mfma_f32_16x16x128_f8f6f4 v[70:73], v[2:9], v[228:235], v[70:73]
	v_mfma_f32_16x16x128_f8f6f4 v[66:69], v[172:179], v[228:235], v[66:69]
	v_mfma_f32_16x16x128_f8f6f4 v[46:49], v[2:9], v[236:243], v[46:49]
	v_mfma_f32_16x16x128_f8f6f4 v[42:45], v[172:179], v[236:243], v[42:45]
	v_mfma_f32_16x16x128_f8f6f4 v[38:41], v[2:9], v[244:251], v[38:41]
	v_mfma_f32_16x16x128_f8f6f4 v[34:37], v[172:179], v[244:251], v[34:37]
	s_setprio 0
	s_barrier
	s_add_i32 s51, s51, 2
	s_add_u32 s49, s49, 0x100
	s_addc_u32 s50, s50, 0
	s_add_u32 s20, s20, 0x100
	s_addc_u32 s21, s21, 0
	s_cmp_lt_u32 s51, 14
	s_cbranch_scc1 .LBB0_1374
	s_andn2_b64 vcc, exec, s[8:9]
	s_cbranch_vccnz .LBB0_1377
	s_barrier
